# LayerNorm wave reductions in ln1_router and combine_ln2: cross-row step via v_permlane16_swap instead of LDS bpermute
# baseline (speedup 1.0000x reference)
.LBB0_1387:
	s_lshl_b32 s9, s12, 6
	v_add_u32_e32 v2, s9, v190
	v_ashrrev_i32_e32 v3, 31, v2
	v_lshlrev_b64 v[186:187], 11, v[2:3]
	v_lshl_add_u64 v[4:5], v[50:51], 0, v[186:187]
	s_barrier
	v_lshl_add_u64 v[6:7], v[52:53], 0, v[186:187]
	global_load_dwordx2 v[182:183], v[4:5], off
	global_load_dwordx2 v[184:185], v[4:5], off offset:512
	global_load_dwordx2 v[200:201], v[4:5], off offset:1024
	global_load_dwordx2 v[202:203], v[4:5], off offset:1536
	global_load_dwordx2 v[210:211], v[6:7], off
	global_load_dwordx2 v[218:219], v[6:7], off offset:512
	global_load_dwordx2 v[220:221], v[6:7], off offset:1024
	global_load_dwordx2 v[224:225], v[6:7], off offset:1536
	v_or_b32_e32 v4, 1, v2
	v_ashrrev_i32_e32 v5, 31, v4
	v_lshlrev_b64 v[164:165], 11, v[4:5]
	v_lshl_add_u64 v[4:5], v[50:51], 0, v[164:165]
	v_lshl_add_u64 v[6:7], v[52:53], 0, v[164:165]
	global_load_dwordx2 v[170:171], v[4:5], off
	global_load_dwordx2 v[178:179], v[4:5], off offset:512
	global_load_dwordx2 v[166:167], v[4:5], off offset:1024
	global_load_dwordx2 v[174:175], v[4:5], off offset:1536
	global_load_dwordx2 v[172:173], v[6:7], off
	global_load_dwordx2 v[180:181], v[6:7], off offset:512
	global_load_dwordx2 v[168:169], v[6:7], off offset:1024
	global_load_dwordx2 v[176:177], v[6:7], off offset:1536
	v_or_b32_e32 v4, 2, v2
	v_ashrrev_i32_e32 v5, 31, v4
	v_lshlrev_b64 v[146:147], 11, v[4:5]
	v_lshl_add_u64 v[4:5], v[50:51], 0, v[146:147]
	v_lshl_add_u64 v[6:7], v[52:53], 0, v[146:147]
	global_load_dwordx2 v[152:153], v[4:5], off
	global_load_dwordx2 v[160:161], v[4:5], off offset:512
	global_load_dwordx2 v[148:149], v[4:5], off offset:1024
	global_load_dwordx2 v[156:157], v[4:5], off offset:1536
	global_load_dwordx2 v[154:155], v[6:7], off
	global_load_dwordx2 v[162:163], v[6:7], off offset:512
	global_load_dwordx2 v[150:151], v[6:7], off offset:1024
	global_load_dwordx2 v[158:159], v[6:7], off offset:1536
	v_or_b32_e32 v4, 3, v2
	v_ashrrev_i32_e32 v5, 31, v4
	v_lshlrev_b64 v[128:129], 11, v[4:5]
	s_mov_b32 s2, 0x3fd744fd
	v_lshl_add_u64 v[4:5], v[50:51], 0, v[128:129]
	v_lshl_add_u64 v[6:7], v[52:53], 0, v[128:129]
	global_load_dwordx2 v[134:135], v[4:5], off
	global_load_dwordx2 v[142:143], v[4:5], off offset:512
	global_load_dwordx2 v[130:131], v[4:5], off offset:1024
	global_load_dwordx2 v[138:139], v[4:5], off offset:1536
	global_load_dwordx2 v[136:137], v[6:7], off
	global_load_dwordx2 v[144:145], v[6:7], off offset:512
	global_load_dwordx2 v[132:133], v[6:7], off offset:1024
	global_load_dwordx2 v[140:141], v[6:7], off offset:1536
	v_or_b32_e32 v4, 4, v2
	v_ashrrev_i32_e32 v5, 31, v4
	v_lshlrev_b64 v[110:111], 11, v[4:5]
	v_lshl_add_u64 v[4:5], v[50:51], 0, v[110:111]
	v_lshl_add_u64 v[6:7], v[52:53], 0, v[110:111]
	global_load_dwordx2 v[116:117], v[4:5], off
	global_load_dwordx2 v[124:125], v[4:5], off offset:512
	global_load_dwordx2 v[112:113], v[4:5], off offset:1024
	global_load_dwordx2 v[120:121], v[4:5], off offset:1536
	global_load_dwordx2 v[118:119], v[6:7], off
	global_load_dwordx2 v[126:127], v[6:7], off offset:512
	global_load_dwordx2 v[114:115], v[6:7], off offset:1024
	global_load_dwordx2 v[122:123], v[6:7], off offset:1536
	v_or_b32_e32 v4, 5, v2
	v_ashrrev_i32_e32 v5, 31, v4
	v_lshlrev_b64 v[92:93], 11, v[4:5]
	v_lshl_add_u64 v[4:5], v[50:51], 0, v[92:93]
	v_lshl_add_u64 v[6:7], v[52:53], 0, v[92:93]
	global_load_dwordx2 v[98:99], v[4:5], off
	global_load_dwordx2 v[106:107], v[4:5], off offset:512
	global_load_dwordx2 v[94:95], v[4:5], off offset:1024
	global_load_dwordx2 v[102:103], v[4:5], off offset:1536
	global_load_dwordx2 v[100:101], v[6:7], off
	global_load_dwordx2 v[108:109], v[6:7], off offset:512
	global_load_dwordx2 v[96:97], v[6:7], off offset:1024
	global_load_dwordx2 v[104:105], v[6:7], off offset:1536
	v_or_b32_e32 v4, 6, v2
	v_ashrrev_i32_e32 v5, 31, v4
	v_or_b32_e32 v2, 7, v2
	v_lshlrev_b64 v[74:75], 11, v[4:5]
	v_ashrrev_i32_e32 v3, 31, v2
	v_lshl_add_u64 v[4:5], v[50:51], 0, v[74:75]
	v_lshlrev_b64 v[56:57], 11, v[2:3]
	v_lshl_add_u64 v[6:7], v[52:53], 0, v[74:75]
	global_load_dwordx2 v[80:81], v[4:5], off
	global_load_dwordx2 v[88:89], v[4:5], off offset:512
	global_load_dwordx2 v[76:77], v[4:5], off offset:1024
	global_load_dwordx2 v[84:85], v[4:5], off offset:1536
	global_load_dwordx2 v[82:83], v[6:7], off
	global_load_dwordx2 v[90:91], v[6:7], off offset:512
	global_load_dwordx2 v[78:79], v[6:7], off offset:1024
	global_load_dwordx2 v[86:87], v[6:7], off offset:1536
	v_lshl_add_u64 v[2:3], v[50:51], 0, v[56:57]
	v_lshl_add_u64 v[4:5], v[52:53], 0, v[56:57]
	global_load_dwordx2 v[62:63], v[2:3], off
	global_load_dwordx2 v[70:71], v[2:3], off offset:512
	global_load_dwordx2 v[58:59], v[2:3], off offset:1024
	global_load_dwordx2 v[66:67], v[2:3], off offset:1536
	global_load_dwordx2 v[64:65], v[4:5], off
	global_load_dwordx2 v[72:73], v[4:5], off offset:512
	global_load_dwordx2 v[60:61], v[4:5], off offset:1024
	global_load_dwordx2 v[68:69], v[4:5], off offset:1536
	global_load_dwordx4 v[26:29], v[44:45], off
	global_load_dwordx4 v[18:21], v[44:45], off offset:1024
	global_load_dwordx4 v[30:33], v[46:47], off
	global_load_dwordx4 v[22:25], v[46:47], off offset:1024
	global_load_dwordx4 v[10:13], v[44:45], off offset:2048
	global_load_dwordx4 v[2:5], v[44:45], off offset:3072
	global_load_dwordx4 v[14:17], v[46:47], off offset:2048
	global_load_dwordx4 v[6:9], v[46:47], off offset:3072
	v_lshl_add_u64 v[186:187], v[54:55], 0, v[186:187]
	v_lshl_add_u64 v[164:165], v[54:55], 0, v[164:165]
	v_lshl_add_u64 v[146:147], v[54:55], 0, v[146:147]
	v_lshl_add_u64 v[128:129], v[54:55], 0, v[128:129]
	v_lshl_add_u64 v[110:111], v[54:55], 0, v[110:111]
	v_lshl_add_u64 v[92:93], v[54:55], 0, v[92:93]
	v_lshl_add_u64 v[74:75], v[54:55], 0, v[74:75]
	v_lshl_add_u64 v[56:57], v[54:55], 0, v[56:57]
	s_waitcnt vmcnt(62)
	v_lshlrev_b32_e32 v232, 16, v183
	v_and_b32_e32 v233, 0xffff0000, v183
	v_lshlrev_b32_e32 v226, 16, v184
	v_and_b32_e32 v227, 0xffff0000, v184
	v_lshlrev_b32_e32 v234, 16, v211
	v_and_b32_e32 v235, 0xffff0000, v211
	v_pk_fma_f32 v[232:233], v[232:233], s[2:3], v[234:235] op_sel_hi:[1,0,1]
	v_lshlrev_b32_e32 v234, 16, v182
	v_and_b32_e32 v235, 0xffff0000, v182
	v_lshlrev_b32_e32 v182, 16, v210
	v_and_b32_e32 v183, 0xffff0000, v210
	v_lshlrev_b32_e32 v228, 16, v218
	v_and_b32_e32 v229, 0xffff0000, v218
	v_and_b32_e32 v184, 0xffff0000, v185
	v_lshlrev_b32_e32 v185, 16, v185
	v_and_b32_e32 v218, 0xffff0000, v219
	v_lshlrev_b32_e32 v219, 16, v219
	v_pk_fma_f32 v[182:183], v[234:235], s[2:3], v[182:183] op_sel_hi:[1,0,1]
	v_pk_fma_f32 v[226:227], v[226:227], s[2:3], v[228:229] op_sel_hi:[1,0,1]
	v_pk_fma_f32 v[184:185], v[184:185], s[2:3], v[218:219] op_sel_hi:[1,0,1]
	v_lshlrev_b32_e32 v199, 16, v202
	v_and_b32_e32 v202, 0xffff0000, v202
	v_mov_b32_e32 v210, v182
	v_mov_b32_e32 v211, v233
	v_pk_mov_b32 v[234:235], v[182:183], v[232:233] op_sel:[1,0]
	v_mul_f32_e32 v202, 0x3fd744fd, v202
	v_and_b32_e32 v209, 0xffff0000, v224
	v_pk_add_f32 v[210:211], v[210:211], v[234:235]
	v_pk_add_f32 v[234:235], v[226:227], v[226:227] op_sel:[0,1] op_sel_hi:[1,0]
	v_pk_add_f32 v[236:237], v[184:185], v[184:185] op_sel:[0,1] op_sel_hi:[1,0]
	v_mov_b32_e32 v235, v202
	v_mov_b32_e32 v237, v209
	v_pk_add_f32 v[234:235], v[234:235], v[236:237]
	v_lshlrev_b32_e32 v236, 16, v201
	v_and_b32_e32 v237, 0xffff0000, v201
	v_lshlrev_b32_e32 v238, 16, v221
	v_and_b32_e32 v239, 0xffff0000, v221
	v_lshlrev_b32_e32 v218, 16, v203
	v_pk_fma_f32 v[236:237], v[236:237], s[2:3], v[238:239] op_sel_hi:[1,0,1]
	v_mul_f32_e32 v229, 0x3fd744fd, v218
	v_lshlrev_b32_e32 v231, 16, v225
	v_mov_b32_e32 v228, v237
	v_mov_b32_e32 v230, v236
	v_pk_add_f32 v[228:229], v[228:229], v[230:231]
	v_lshlrev_b32_e32 v230, 16, v200
	v_and_b32_e32 v231, 0xffff0000, v200
	v_lshlrev_b32_e32 v200, 16, v220
	v_and_b32_e32 v201, 0xffff0000, v220
	v_mul_f32_e32 v199, 0x3fd744fd, v199
	v_and_b32_e32 v203, 0xffff0000, v203
	v_pk_add_f32 v[210:211], v[210:211], v[210:211] op_sel:[0,1] op_sel_hi:[1,0]
	v_pk_fma_f32 v[200:201], v[230:231], s[2:3], v[200:201] op_sel_hi:[1,0,1]
	v_lshlrev_b32_e32 v219, 16, v224
	v_mul_f32_e32 v203, 0x3fd744fd, v203
	v_and_b32_e32 v225, 0xffff0000, v225
	v_mov_b32_e32 v211, v199
	v_mov_b32_e32 v218, v1
	v_mov_b32_e32 v202, v200
	v_mov_b32_e32 v224, v201
	v_pk_add_f32 v[210:211], v[210:211], v[218:219]
	v_pk_add_f32 v[202:203], v[202:203], v[224:225]
	v_pk_add_f32 v[218:219], v[210:211], v[234:235]
	v_pk_add_f32 v[220:221], v[202:203], v[228:229]
	v_mov_b32_e32 v234, v211
	v_pk_add_f32 v[218:219], v[218:219], v[220:221]
	s_nop 0
	v_add_f32_e32 v199, v218, v219
	s_nop 1
	v_add_f32_dpp v199, v199, v199 quad_perm:[1,0,3,2] row_mask:0xf bank_mask:0xf bound_ctrl:1
	s_nop 1
	v_add_f32_dpp v199, v199, v199 quad_perm:[2,3,0,1] row_mask:0xf bank_mask:0xf bound_ctrl:1
	s_nop 1
	v_add_f32_dpp v199, v199, v199 row_half_mirror row_mask:0xf bank_mask:0xf bound_ctrl:1
	s_nop 1
	v_add_f32_dpp v199, v199, v199 row_mirror row_mask:0xf bank_mask:0xf bound_ctrl:1
	v_mov_b32_e32 v202, v199
	s_nop 1
	v_permlane32_swap_b32 v199, v202
	s_nop 0
	v_add_f32_e32 v199, v199, v202
	v_mov_b32_e32 v202, v199
	s_nop 1
	v_permlane16_swap_b32_e32 v199, v202
	s_waitcnt lgkmcnt(0)
	v_add_f32_e32 v199, v199, v202
	v_mul_f32_e32 v210, 0x3a800000, v199
	v_pk_add_f32 v[182:183], v[182:183], v[210:211] op_sel_hi:[1,0] neg_lo:[0,1] neg_hi:[0,1]
	v_pk_add_f32 v[220:221], v[232:233], v[210:211] op_sel_hi:[1,0] neg_lo:[0,1] neg_hi:[0,1]
	v_pk_mul_f32 v[218:219], v[182:183], v[182:183]
	v_pk_mul_f32 v[224:225], v[220:221], v[220:221]
	v_add_f32_e32 v199, v218, v219
	v_pk_add_f32 v[226:227], v[226:227], v[210:211] op_sel_hi:[1,0] neg_lo:[0,1] neg_hi:[0,1]
	v_add_f32_e32 v199, v224, v199
	v_pk_mul_f32 v[240:241], v[226:227], v[226:227]
	v_add_f32_e32 v199, v225, v199
	v_pk_add_f32 v[184:185], v[184:185], v[210:211] op_sel_hi:[1,0] neg_lo:[0,1] neg_hi:[0,1]
	v_add_f32_e32 v199, v240, v199
	v_pk_mul_f32 v[238:239], v[184:185], v[184:185]
	v_add_f32_e32 v199, v241, v199
	v_pk_add_f32 v[200:201], v[200:201], v[210:211] op_sel_hi:[1,0] neg_lo:[0,1] neg_hi:[0,1]
	v_add_f32_e32 v199, v239, v199
	v_pk_mul_f32 v[230:231], v[200:201], v[200:201]
	v_add_f32_e32 v199, v238, v199
	v_pk_add_f32 v[232:233], v[236:237], v[210:211] op_sel_hi:[1,0] neg_lo:[0,1] neg_hi:[0,1]
	v_add_f32_e32 v199, v230, v199
	v_pk_mul_f32 v[236:237], v[232:233], v[232:233]
	v_mov_b32_e32 v202, v229
	v_add_f32_e32 v199, v231, v199
	v_pk_add_f32 v[202:203], v[202:203], v[210:211] op_sel_hi:[1,0] neg_lo:[0,1] neg_hi:[0,1]
	v_pk_add_f32 v[210:211], v[234:235], v[210:211] op_sel_hi:[1,0] neg_lo:[0,1] neg_hi:[0,1]
	v_add_f32_e32 v199, v236, v199
	v_pk_mul_f32 v[234:235], v[210:211], v[210:211]
	v_add_f32_e32 v199, v237, v199
	v_add_f32_e32 v199, v234, v199
	v_pk_mul_f32 v[228:229], v[202:203], v[202:203]
	v_add_f32_e32 v199, v235, v199
	v_add_f32_e32 v199, v228, v199
	v_add_f32_e32 v199, v229, v199
	s_nop 1
	v_add_f32_dpp v199, v199, v199 quad_perm:[1,0,3,2] row_mask:0xf bank_mask:0xf bound_ctrl:1
	s_nop 1
	v_add_f32_dpp v199, v199, v199 quad_perm:[2,3,0,1] row_mask:0xf bank_mask:0xf bound_ctrl:1
	s_nop 1
	v_add_f32_dpp v199, v199, v199 row_half_mirror row_mask:0xf bank_mask:0xf bound_ctrl:1
	s_nop 1
	v_add_f32_dpp v199, v199, v199 row_mirror row_mask:0xf bank_mask:0xf bound_ctrl:1
	v_mov_b32_e32 v209, v199
	s_nop 1
	v_permlane32_swap_b32 v199, v209
	s_nop 0
	v_add_f32_e32 v199, v199, v209
	v_mov_b32_e32 v209, v199
	s_nop 1
	v_permlane16_swap_b32_e32 v199, v209
	s_waitcnt lgkmcnt(0)
	v_add_f32_e32 v199, v199, v209
	v_fmamk_f32 v199, v199, 0x3a800000, v206
	v_mul_f32_e32 v209, 0x4f800000, v199
	v_cmp_gt_f32_e32 vcc, s45, v199
	s_nop 1
	v_cndmask_b32_e32 v199, v199, v209, vcc
	v_sqrt_f32_e32 v209, v199
	s_nop 0
	v_add_u32_e32 v218, -1, v209
	v_fma_f32 v219, -v218, v209, v199
	v_cmp_ge_f32_e64 s[0:1], 0, v219
	v_add_u32_e32 v219, 1, v209
	s_nop 0
	v_cndmask_b32_e64 v218, v209, v218, s[0:1]
	v_fma_f32 v209, -v219, v209, v199
	v_cmp_lt_f32_e64 s[0:1], 0, v209
	s_nop 1
	v_cndmask_b32_e64 v209, v218, v219, s[0:1]
	v_mul_f32_e32 v218, 0x37800000, v209
	v_cndmask_b32_e32 v209, v209, v218, vcc
	v_cmp_class_f32_e32 vcc, v199, v207
	s_nop 1
	v_cndmask_b32_e32 v199, v209, v199, vcc
	v_div_scale_f32 v209, s[0:1], v199, v199, 1.0
	v_rcp_f32_e32 v218, v209
	s_nop 0
	v_fma_f32 v219, -v209, v218, 1.0
	v_fmac_f32_e32 v218, v219, v218
	v_div_scale_f32 v219, vcc, 1.0, v199, 1.0
	v_mul_f32_e32 v223, v219, v218
	v_fma_f32 v224, -v209, v223, v219
	v_fmac_f32_e32 v223, v224, v218
	v_fma_f32 v209, -v209, v223, v219
	v_div_fmas_f32 v209, v209, v218, v223
	v_div_fixup_f32 v218, v209, v199, 1.0
	v_pk_mul_f32 v[182:183], v[182:183], v[218:219] op_sel_hi:[1,0]
	v_pk_mul_f32 v[220:221], v[220:221], v[218:219] op_sel_hi:[1,0]
	s_waitcnt vmcnt(5)
	v_pk_fma_f32 v[182:183], v[26:27], v[182:183], v[30:31]
	v_pk_fma_f32 v[220:221], v[28:29], v[220:221], v[32:33]
	v_cvt_pk_bf16_f32 v182, v182, v183
	v_cvt_pk_bf16_f32 v183, v220, v221
	v_pk_mul_f32 v[220:221], v[226:227], v[218:219] op_sel_hi:[1,0]
	v_pk_mul_f32 v[184:185], v[184:185], v[218:219] op_sel_hi:[1,0]
	s_waitcnt vmcnt(4)
	v_pk_fma_f32 v[220:221], v[18:19], v[220:221], v[22:23]
	v_pk_fma_f32 v[184:185], v[20:21], v[184:185], v[24:25] op_sel:[0,1,0] op_sel_hi:[1,0,1]
	v_cvt_pk_bf16_f32 v220, v220, v221
	v_cvt_pk_bf16_f32 v221, v184, v185
	global_store_dwordx2 v[186:187], v[182:183], off
	ds_write2st64_b64 v195, v[182:183], v[220:221] offset0:32 offset1:33
	v_pk_mul_f32 v[182:183], v[200:201], v[218:219] op_sel_hi:[1,0]
	v_pk_mul_f32 v[184:185], v[232:233], v[218:219] op_sel_hi:[1,0]
	s_waitcnt vmcnt(2)
	v_pk_fma_f32 v[182:183], v[10:11], v[182:183], v[14:15]
	v_pk_fma_f32 v[184:185], v[12:13], v[184:185], v[16:17]
	v_cvt_pk_bf16_f32 v182, v182, v183
	v_cvt_pk_bf16_f32 v183, v184, v185
	v_pk_mul_f32 v[184:185], v[210:211], v[218:219] op_sel_hi:[1,0]
	v_pk_mul_f32 v[200:201], v[202:203], v[218:219] op_sel_hi:[1,0]
	s_waitcnt vmcnt(1)
	v_pk_fma_f32 v[184:185], v[2:3], v[184:185], v[6:7]
	v_pk_fma_f32 v[200:201], v[4:5], v[200:201], v[8:9]
	v_cvt_pk_bf16_f32 v184, v184, v185
	v_cvt_pk_bf16_f32 v185, v200, v201
	v_lshlrev_b32_e32 v200, 16, v171
	v_and_b32_e32 v201, 0xffff0000, v171
	v_lshlrev_b32_e32 v202, 16, v173
	v_and_b32_e32 v203, 0xffff0000, v173
	v_pk_fma_f32 v[200:201], v[200:201], s[2:3], v[202:203] op_sel_hi:[1,0,1]
	v_lshlrev_b32_e32 v202, 16, v170
	v_and_b32_e32 v203, 0xffff0000, v170
	v_lshlrev_b32_e32 v170, 16, v172
	v_and_b32_e32 v171, 0xffff0000, v172
	global_store_dwordx2 v[186:187], v[182:183], off offset:1024
	global_store_dwordx2 v[186:187], v[184:185], off offset:1536
	ds_write2st64_b64 v195, v[182:183], v[184:185] offset0:34 offset1:35
	v_lshlrev_b32_e32 v182, 16, v178
	v_and_b32_e32 v183, 0xffff0000, v178
	v_lshlrev_b32_e32 v184, 16, v180
	v_and_b32_e32 v185, 0xffff0000, v180
	v_and_b32_e32 v178, 0xffff0000, v179
	v_lshlrev_b32_e32 v179, 16, v179
	v_and_b32_e32 v180, 0xffff0000, v181
	v_lshlrev_b32_e32 v181, 16, v181
	v_pk_fma_f32 v[170:171], v[202:203], s[2:3], v[170:171] op_sel_hi:[1,0,1]
	v_pk_fma_f32 v[182:183], v[182:183], s[2:3], v[184:185] op_sel_hi:[1,0,1]
	v_pk_fma_f32 v[178:179], v[178:179], s[2:3], v[180:181] op_sel_hi:[1,0,1]
	v_lshlrev_b32_e32 v180, 16, v174
	v_and_b32_e32 v174, 0xffff0000, v174
	v_mov_b32_e32 v172, v170
	v_mov_b32_e32 v173, v201
	v_pk_mov_b32 v[202:203], v[170:171], v[200:201] op_sel:[1,0]
	v_lshlrev_b32_e32 v181, 16, v176
	v_mul_f32_e32 v174, 0x3fd744fd, v174
	v_and_b32_e32 v176, 0xffff0000, v176
	v_pk_add_f32 v[172:173], v[172:173], v[202:203]
	v_pk_add_f32 v[202:203], v[182:183], v[182:183] op_sel:[0,1] op_sel_hi:[1,0]
	v_pk_add_f32 v[210:211], v[178:179], v[178:179] op_sel:[0,1] op_sel_hi:[1,0]
	v_mov_b32_e32 v203, v174
	v_mov_b32_e32 v211, v176
	v_pk_add_f32 v[202:203], v[202:203], v[210:211]
	v_lshlrev_b32_e32 v210, 16, v167
	v_and_b32_e32 v211, 0xffff0000, v167
	v_lshlrev_b32_e32 v218, 16, v169
	v_and_b32_e32 v219, 0xffff0000, v169
	v_lshlrev_b32_e32 v184, 16, v175
	v_pk_fma_f32 v[210:211], v[210:211], s[2:3], v[218:219] op_sel_hi:[1,0,1]
	global_store_dwordx2 v[186:187], v[220:221], off offset:512
	v_mul_f32_e32 v185, 0x3fd744fd, v184
	v_lshlrev_b32_e32 v187, 16, v177
	v_mov_b32_e32 v184, v211
	v_mov_b32_e32 v186, v210
	v_pk_add_f32 v[184:185], v[184:185], v[186:187]
	v_lshlrev_b32_e32 v186, 16, v166
	v_and_b32_e32 v187, 0xffff0000, v166
	v_lshlrev_b32_e32 v166, 16, v168
	v_and_b32_e32 v167, 0xffff0000, v168
	v_mul_f32_e32 v180, 0x3fd744fd, v180
	v_and_b32_e32 v175, 0xffff0000, v175
	v_pk_add_f32 v[172:173], v[172:173], v[172:173] op_sel:[0,1] op_sel_hi:[1,0]
	v_pk_fma_f32 v[166:167], v[186:187], s[2:3], v[166:167] op_sel_hi:[1,0,1]
	v_mul_f32_e32 v175, 0x3fd744fd, v175
	v_and_b32_e32 v177, 0xffff0000, v177
	v_mov_b32_e32 v173, v180
	v_mov_b32_e32 v180, v1
	v_mov_b32_e32 v174, v166
	v_mov_b32_e32 v176, v167
	v_pk_add_f32 v[172:173], v[172:173], v[180:181]
	v_pk_add_f32 v[168:169], v[174:175], v[176:177]
	v_pk_add_f32 v[180:181], v[172:173], v[202:203]
	v_pk_add_f32 v[174:175], v[168:169], v[184:185]
	v_mov_b32_e32 v202, v173
	v_pk_add_f32 v[174:175], v[180:181], v[174:175]
	s_nop 0
	v_add_f32_e32 v168, v174, v175
	s_nop 1
	v_add_f32_dpp v168, v168, v168 quad_perm:[1,0,3,2] row_mask:0xf bank_mask:0xf bound_ctrl:1
	s_nop 1
	v_add_f32_dpp v168, v168, v168 quad_perm:[2,3,0,1] row_mask:0xf bank_mask:0xf bound_ctrl:1
	s_nop 1
	v_add_f32_dpp v168, v168, v168 row_half_mirror row_mask:0xf bank_mask:0xf bound_ctrl:1
	s_nop 1
	v_add_f32_dpp v168, v168, v168 row_mirror row_mask:0xf bank_mask:0xf bound_ctrl:1
	v_mov_b32_e32 v172, v168
	s_nop 1
	v_permlane32_swap_b32 v168, v172
	s_nop 0
	v_add_f32_e32 v168, v168, v172
	v_mov_b32_e32 v172, v168
	s_nop 1
	v_permlane16_swap_b32_e32 v168, v172
	s_waitcnt lgkmcnt(0)
	v_add_f32_e32 v168, v168, v172
	v_mul_f32_e32 v172, 0x3a800000, v168
	v_pk_add_f32 v[170:171], v[170:171], v[172:173] op_sel_hi:[1,0] neg_lo:[0,1] neg_hi:[0,1]
	v_pk_add_f32 v[176:177], v[200:201], v[172:173] op_sel_hi:[1,0] neg_lo:[0,1] neg_hi:[0,1]
	v_pk_mul_f32 v[174:175], v[170:171], v[170:171]
	v_pk_mul_f32 v[180:181], v[176:177], v[176:177]
	v_add_f32_e32 v174, v174, v175
	v_pk_add_f32 v[182:183], v[182:183], v[172:173] op_sel_hi:[1,0] neg_lo:[0,1] neg_hi:[0,1]
	v_add_f32_e32 v174, v180, v174
	v_pk_mul_f32 v[220:221], v[182:183], v[182:183]
	v_add_f32_e32 v174, v181, v174
	v_pk_add_f32 v[178:179], v[178:179], v[172:173] op_sel_hi:[1,0] neg_lo:[0,1] neg_hi:[0,1]
	v_add_f32_e32 v174, v220, v174
	v_pk_mul_f32 v[218:219], v[178:179], v[178:179]
	v_add_f32_e32 v174, v221, v174
	v_pk_add_f32 v[166:167], v[166:167], v[172:173] op_sel_hi:[1,0] neg_lo:[0,1] neg_hi:[0,1]
	v_add_f32_e32 v174, v219, v174
	v_pk_mul_f32 v[186:187], v[166:167], v[166:167]
	v_add_f32_e32 v174, v218, v174
	v_pk_add_f32 v[200:201], v[210:211], v[172:173] op_sel_hi:[1,0] neg_lo:[0,1] neg_hi:[0,1]
	v_add_f32_e32 v174, v186, v174
	v_pk_mul_f32 v[210:211], v[200:201], v[200:201]
	v_mov_b32_e32 v168, v185
	v_add_f32_e32 v174, v187, v174
	v_pk_add_f32 v[168:169], v[168:169], v[172:173] op_sel_hi:[1,0] neg_lo:[0,1] neg_hi:[0,1]
	v_pk_add_f32 v[172:173], v[202:203], v[172:173] op_sel_hi:[1,0] neg_lo:[0,1] neg_hi:[0,1]
	v_add_f32_e32 v174, v210, v174
	v_pk_mul_f32 v[202:203], v[172:173], v[172:173]
	v_add_f32_e32 v174, v211, v174
	v_add_f32_e32 v174, v202, v174
	v_pk_mul_f32 v[184:185], v[168:169], v[168:169]
	v_add_f32_e32 v174, v203, v174
	v_add_f32_e32 v174, v184, v174
	v_add_f32_e32 v174, v185, v174
	s_nop 1
	v_add_f32_dpp v174, v174, v174 quad_perm:[1,0,3,2] row_mask:0xf bank_mask:0xf bound_ctrl:1
	s_nop 1
	v_add_f32_dpp v174, v174, v174 quad_perm:[2,3,0,1] row_mask:0xf bank_mask:0xf bound_ctrl:1
	s_nop 1
	v_add_f32_dpp v174, v174, v174 row_half_mirror row_mask:0xf bank_mask:0xf bound_ctrl:1
	s_nop 1
	v_add_f32_dpp v174, v174, v174 row_mirror row_mask:0xf bank_mask:0xf bound_ctrl:1
	v_mov_b32_e32 v175, v174
	s_nop 1
	v_permlane32_swap_b32 v174, v175
	s_nop 0
	v_add_f32_e32 v174, v174, v175
	v_mov_b32_e32 v175, v174
	s_nop 1
	v_permlane16_swap_b32_e32 v174, v175
	s_waitcnt lgkmcnt(0)
	v_add_f32_e32 v174, v174, v175
	v_fmamk_f32 v174, v174, 0x3a800000, v206
	v_mul_f32_e32 v175, 0x4f800000, v174
	v_cmp_gt_f32_e32 vcc, s45, v174
	s_nop 1
	v_cndmask_b32_e32 v174, v174, v175, vcc
	v_sqrt_f32_e32 v175, v174
	s_nop 0
	v_add_u32_e32 v180, -1, v175
	v_fma_f32 v181, -v180, v175, v174
	v_cmp_ge_f32_e64 s[0:1], 0, v181
	v_add_u32_e32 v181, 1, v175
	s_nop 0
	v_cndmask_b32_e64 v180, v175, v180, s[0:1]
	v_fma_f32 v175, -v181, v175, v174
	v_cmp_lt_f32_e64 s[0:1], 0, v175
	s_nop 1
	v_cndmask_b32_e64 v175, v180, v181, s[0:1]
	v_mul_f32_e32 v180, 0x37800000, v175
	v_cndmask_b32_e32 v175, v175, v180, vcc
	v_cmp_class_f32_e32 vcc, v174, v207
	s_nop 1
	v_cndmask_b32_e32 v174, v175, v174, vcc
	v_div_scale_f32 v175, s[0:1], v174, v174, 1.0
	v_rcp_f32_e32 v180, v175
	s_nop 0
	v_fma_f32 v181, -v175, v180, 1.0
	v_fmac_f32_e32 v180, v181, v180
	v_div_scale_f32 v181, vcc, 1.0, v174, 1.0
	v_mul_f32_e32 v184, v181, v180
	v_fma_f32 v185, -v175, v184, v181
	v_fmac_f32_e32 v184, v185, v180
	v_fma_f32 v175, -v175, v184, v181
	v_div_fmas_f32 v175, v175, v180, v184
	v_div_fixup_f32 v174, v175, v174, 1.0
	v_pk_mul_f32 v[170:171], v[170:171], v[174:175] op_sel_hi:[1,0]
	v_pk_mul_f32 v[176:177], v[176:177], v[174:175] op_sel_hi:[1,0]
	v_pk_fma_f32 v[170:171], v[26:27], v[170:171], v[30:31]
	v_pk_fma_f32 v[176:177], v[28:29], v[176:177], v[32:33]
	v_cvt_pk_bf16_f32 v170, v170, v171
	v_cvt_pk_bf16_f32 v171, v176, v177
	v_pk_mul_f32 v[176:177], v[182:183], v[174:175] op_sel_hi:[1,0]
	v_pk_mul_f32 v[178:179], v[178:179], v[174:175] op_sel_hi:[1,0]
	v_pk_fma_f32 v[176:177], v[18:19], v[176:177], v[22:23]
	v_pk_fma_f32 v[178:179], v[20:21], v[178:179], v[24:25] op_sel:[0,1,0] op_sel_hi:[1,0,1]
	v_cvt_pk_bf16_f32 v176, v176, v177
	v_cvt_pk_bf16_f32 v177, v178, v179
	v_add_u32_e32 v175, 16, v195
	global_store_dwordx2 v[164:165], v[170:171], off
	ds_write2st64_b64 v175, v[170:171], v[176:177] offset0:36 offset1:37
	v_pk_mul_f32 v[166:167], v[166:167], v[174:175] op_sel_hi:[1,0]
	v_pk_mul_f32 v[170:171], v[200:201], v[174:175] op_sel_hi:[1,0]
	v_pk_fma_f32 v[166:167], v[10:11], v[166:167], v[14:15]
	v_pk_fma_f32 v[170:171], v[12:13], v[170:171], v[16:17]
	v_cvt_pk_bf16_f32 v166, v166, v167
	v_cvt_pk_bf16_f32 v167, v170, v171
	v_pk_mul_f32 v[170:171], v[172:173], v[174:175] op_sel_hi:[1,0]
	v_pk_mul_f32 v[168:169], v[168:169], v[174:175] op_sel_hi:[1,0]
	v_pk_fma_f32 v[170:171], v[2:3], v[170:171], v[6:7]
	v_pk_fma_f32 v[168:169], v[4:5], v[168:169], v[8:9]
	v_cvt_pk_bf16_f32 v170, v170, v171
	v_cvt_pk_bf16_f32 v171, v168, v169
	global_store_dwordx2 v[164:165], v[170:171], off offset:1536
	ds_write2st64_b64 v175, v[166:167], v[170:171] offset0:38 offset1:39
	v_lshlrev_b32_e32 v170, 16, v153
	v_and_b32_e32 v171, 0xffff0000, v153
	v_lshlrev_b32_e32 v172, 16, v155
	v_and_b32_e32 v173, 0xffff0000, v155
	v_pk_fma_f32 v[170:171], v[170:171], s[2:3], v[172:173] op_sel_hi:[1,0,1]
	v_lshlrev_b32_e32 v172, 16, v152
	v_and_b32_e32 v173, 0xffff0000, v152
	v_lshlrev_b32_e32 v152, 16, v154
	v_and_b32_e32 v153, 0xffff0000, v154
	global_store_dwordx2 v[164:165], v[176:177], off offset:512
	global_store_dwordx2 v[164:165], v[166:167], off offset:1024
	v_lshlrev_b32_e32 v164, 16, v160
	v_and_b32_e32 v165, 0xffff0000, v160
	v_lshlrev_b32_e32 v166, 16, v162
	v_and_b32_e32 v167, 0xffff0000, v162
	v_and_b32_e32 v160, 0xffff0000, v161
	v_lshlrev_b32_e32 v161, 16, v161
	v_and_b32_e32 v162, 0xffff0000, v163
	v_lshlrev_b32_e32 v163, 16, v163
	v_pk_fma_f32 v[152:153], v[172:173], s[2:3], v[152:153] op_sel_hi:[1,0,1]
	v_pk_fma_f32 v[164:165], v[164:165], s[2:3], v[166:167] op_sel_hi:[1,0,1]
	v_pk_fma_f32 v[160:161], v[160:161], s[2:3], v[162:163] op_sel_hi:[1,0,1]
	v_lshlrev_b32_e32 v162, 16, v156
	v_and_b32_e32 v156, 0xffff0000, v156
	v_mov_b32_e32 v154, v152
	v_mov_b32_e32 v155, v171
	v_pk_mov_b32 v[172:173], v[152:153], v[170:171] op_sel:[1,0]
	v_lshlrev_b32_e32 v163, 16, v158
	v_mul_f32_e32 v156, 0x3fd744fd, v156
	v_and_b32_e32 v158, 0xffff0000, v158
	v_pk_add_f32 v[154:155], v[154:155], v[172:173]
	v_pk_add_f32 v[172:173], v[164:165], v[164:165] op_sel:[0,1] op_sel_hi:[1,0]
	v_pk_add_f32 v[174:175], v[160:161], v[160:161] op_sel:[0,1] op_sel_hi:[1,0]
	v_mov_b32_e32 v173, v156
	v_mov_b32_e32 v175, v158
	v_pk_add_f32 v[172:173], v[172:173], v[174:175]
	v_lshlrev_b32_e32 v174, 16, v149
	v_and_b32_e32 v175, 0xffff0000, v149
	v_lshlrev_b32_e32 v176, 16, v151
	v_and_b32_e32 v177, 0xffff0000, v151
	v_lshlrev_b32_e32 v166, 16, v157
	v_pk_fma_f32 v[174:175], v[174:175], s[2:3], v[176:177] op_sel_hi:[1,0,1]
	v_mul_f32_e32 v167, 0x3fd744fd, v166
	v_lshlrev_b32_e32 v169, 16, v159
	v_mov_b32_e32 v166, v175
	v_mov_b32_e32 v168, v174
	v_pk_add_f32 v[166:167], v[166:167], v[168:169]
	v_lshlrev_b32_e32 v168, 16, v148
	v_and_b32_e32 v169, 0xffff0000, v148
	v_lshlrev_b32_e32 v148, 16, v150
	v_and_b32_e32 v149, 0xffff0000, v150
	v_mul_f32_e32 v162, 0x3fd744fd, v162
	v_and_b32_e32 v157, 0xffff0000, v157
	v_pk_add_f32 v[154:155], v[154:155], v[154:155] op_sel:[0,1] op_sel_hi:[1,0]
	v_pk_fma_f32 v[148:149], v[168:169], s[2:3], v[148:149] op_sel_hi:[1,0,1]
	v_mul_f32_e32 v157, 0x3fd744fd, v157
	v_and_b32_e32 v159, 0xffff0000, v159
	v_mov_b32_e32 v155, v162
	v_mov_b32_e32 v162, v1
	v_mov_b32_e32 v156, v148
	v_mov_b32_e32 v158, v149
	v_pk_add_f32 v[154:155], v[154:155], v[162:163]
	v_pk_add_f32 v[150:151], v[156:157], v[158:159]
	v_pk_add_f32 v[162:163], v[154:155], v[172:173]
	v_pk_add_f32 v[156:157], v[150:151], v[166:167]
	v_mov_b32_e32 v172, v155
	v_pk_add_f32 v[156:157], v[162:163], v[156:157]
	s_nop 0
	v_add_f32_e32 v150, v156, v157
	s_nop 1
	v_add_f32_dpp v150, v150, v150 quad_perm:[1,0,3,2] row_mask:0xf bank_mask:0xf bound_ctrl:1
	s_nop 1
	v_add_f32_dpp v150, v150, v150 quad_perm:[2,3,0,1] row_mask:0xf bank_mask:0xf bound_ctrl:1
	s_nop 1
	v_add_f32_dpp v150, v150, v150 row_half_mirror row_mask:0xf bank_mask:0xf bound_ctrl:1
	s_nop 1
	v_add_f32_dpp v150, v150, v150 row_mirror row_mask:0xf bank_mask:0xf bound_ctrl:1
	v_mov_b32_e32 v154, v150
	s_nop 1
	v_permlane32_swap_b32 v150, v154
	s_nop 0
	v_add_f32_e32 v150, v150, v154
	v_mov_b32_e32 v154, v150
	s_nop 1
	v_permlane16_swap_b32_e32 v150, v154
	s_waitcnt lgkmcnt(0)
	v_add_f32_e32 v150, v150, v154
	v_mul_f32_e32 v154, 0x3a800000, v150
	v_pk_add_f32 v[152:153], v[152:153], v[154:155] op_sel_hi:[1,0] neg_lo:[0,1] neg_hi:[0,1]
	v_pk_add_f32 v[158:159], v[170:171], v[154:155] op_sel_hi:[1,0] neg_lo:[0,1] neg_hi:[0,1]
	v_pk_mul_f32 v[156:157], v[152:153], v[152:153]
	v_pk_mul_f32 v[162:163], v[158:159], v[158:159]
	v_add_f32_e32 v156, v156, v157
	v_pk_add_f32 v[164:165], v[164:165], v[154:155] op_sel_hi:[1,0] neg_lo:[0,1] neg_hi:[0,1]
	v_add_f32_e32 v156, v162, v156
	v_pk_mul_f32 v[178:179], v[164:165], v[164:165]
	v_add_f32_e32 v156, v163, v156
	v_pk_add_f32 v[160:161], v[160:161], v[154:155] op_sel_hi:[1,0] neg_lo:[0,1] neg_hi:[0,1]
	v_add_f32_e32 v156, v178, v156
	v_pk_mul_f32 v[176:177], v[160:161], v[160:161]
	v_add_f32_e32 v156, v179, v156
	v_pk_add_f32 v[148:149], v[148:149], v[154:155] op_sel_hi:[1,0] neg_lo:[0,1] neg_hi:[0,1]
	v_add_f32_e32 v156, v177, v156
	v_pk_mul_f32 v[168:169], v[148:149], v[148:149]
	v_add_f32_e32 v156, v176, v156
	v_pk_add_f32 v[170:171], v[174:175], v[154:155] op_sel_hi:[1,0] neg_lo:[0,1] neg_hi:[0,1]
	v_add_f32_e32 v156, v168, v156
	v_pk_mul_f32 v[174:175], v[170:171], v[170:171]
	v_mov_b32_e32 v150, v167
	v_add_f32_e32 v156, v169, v156
	v_pk_add_f32 v[150:151], v[150:151], v[154:155] op_sel_hi:[1,0] neg_lo:[0,1] neg_hi:[0,1]
	v_pk_add_f32 v[154:155], v[172:173], v[154:155] op_sel_hi:[1,0] neg_lo:[0,1] neg_hi:[0,1]
	v_add_f32_e32 v156, v174, v156
	v_pk_mul_f32 v[172:173], v[154:155], v[154:155]
	v_add_f32_e32 v156, v175, v156
	v_add_f32_e32 v156, v172, v156
	v_pk_mul_f32 v[166:167], v[150:151], v[150:151]
	v_add_f32_e32 v156, v173, v156
	v_add_f32_e32 v156, v166, v156
	v_add_f32_e32 v156, v167, v156
	s_nop 1
	v_add_f32_dpp v156, v156, v156 quad_perm:[1,0,3,2] row_mask:0xf bank_mask:0xf bound_ctrl:1
	s_nop 1
	v_add_f32_dpp v156, v156, v156 quad_perm:[2,3,0,1] row_mask:0xf bank_mask:0xf bound_ctrl:1
	s_nop 1
	v_add_f32_dpp v156, v156, v156 row_half_mirror row_mask:0xf bank_mask:0xf bound_ctrl:1
	s_nop 1
	v_add_f32_dpp v156, v156, v156 row_mirror row_mask:0xf bank_mask:0xf bound_ctrl:1
	v_mov_b32_e32 v157, v156
	s_nop 1
	v_permlane32_swap_b32 v156, v157
	s_nop 0
	v_add_f32_e32 v156, v156, v157
	v_mov_b32_e32 v157, v156
	s_nop 1
	v_permlane16_swap_b32_e32 v156, v157
	s_waitcnt lgkmcnt(0)
	v_add_f32_e32 v156, v156, v157
	v_fmamk_f32 v156, v156, 0x3a800000, v206
	v_mul_f32_e32 v157, 0x4f800000, v156
	v_cmp_gt_f32_e32 vcc, s45, v156
	s_nop 1
	v_cndmask_b32_e32 v156, v156, v157, vcc
	v_sqrt_f32_e32 v157, v156
	s_nop 0
	v_add_u32_e32 v162, -1, v157
	v_fma_f32 v163, -v162, v157, v156
	v_cmp_ge_f32_e64 s[0:1], 0, v163
	v_add_u32_e32 v163, 1, v157
	s_nop 0
	v_cndmask_b32_e64 v162, v157, v162, s[0:1]
	v_fma_f32 v157, -v163, v157, v156
	v_cmp_lt_f32_e64 s[0:1], 0, v157
	s_nop 1
	v_cndmask_b32_e64 v157, v162, v163, s[0:1]
	v_mul_f32_e32 v162, 0x37800000, v157
	v_cndmask_b32_e32 v157, v157, v162, vcc
	v_cmp_class_f32_e32 vcc, v156, v207
	s_nop 1
	v_cndmask_b32_e32 v156, v157, v156, vcc
	v_div_scale_f32 v157, s[0:1], v156, v156, 1.0
	v_rcp_f32_e32 v162, v157
	s_nop 0
	v_fma_f32 v163, -v157, v162, 1.0
	v_fmac_f32_e32 v162, v163, v162
	v_div_scale_f32 v163, vcc, 1.0, v156, 1.0
	v_mul_f32_e32 v166, v163, v162
	v_fma_f32 v167, -v157, v166, v163
	v_fmac_f32_e32 v166, v167, v162
	v_fma_f32 v157, -v157, v166, v163
	v_div_fmas_f32 v157, v157, v162, v166
	v_div_fixup_f32 v156, v157, v156, 1.0
	v_pk_mul_f32 v[152:153], v[152:153], v[156:157] op_sel_hi:[1,0]
	v_pk_mul_f32 v[158:159], v[158:159], v[156:157] op_sel_hi:[1,0]
	v_pk_fma_f32 v[152:153], v[26:27], v[152:153], v[30:31]
	v_pk_fma_f32 v[158:159], v[28:29], v[158:159], v[32:33]
	v_cvt_pk_bf16_f32 v152, v152, v153
	v_cvt_pk_bf16_f32 v153, v158, v159
	v_pk_mul_f32 v[158:159], v[164:165], v[156:157] op_sel_hi:[1,0]
	v_pk_mul_f32 v[160:161], v[160:161], v[156:157] op_sel_hi:[1,0]
	v_pk_fma_f32 v[158:159], v[18:19], v[158:159], v[22:23]
	v_pk_fma_f32 v[160:161], v[20:21], v[160:161], v[24:25] op_sel:[0,1,0] op_sel_hi:[1,0,1]
	v_cvt_pk_bf16_f32 v158, v158, v159
	v_cvt_pk_bf16_f32 v159, v160, v161
	v_add_u32_e32 v157, 32, v195
	global_store_dwordx2 v[146:147], v[152:153], off
	ds_write2st64_b64 v157, v[152:153], v[158:159] offset0:40 offset1:41
	v_pk_mul_f32 v[148:149], v[148:149], v[156:157] op_sel_hi:[1,0]
	v_pk_mul_f32 v[152:153], v[170:171], v[156:157] op_sel_hi:[1,0]
	v_pk_fma_f32 v[148:149], v[10:11], v[148:149], v[14:15]
	v_pk_fma_f32 v[152:153], v[12:13], v[152:153], v[16:17]
	v_cvt_pk_bf16_f32 v148, v148, v149
	v_cvt_pk_bf16_f32 v149, v152, v153
	v_pk_mul_f32 v[152:153], v[154:155], v[156:157] op_sel_hi:[1,0]
	v_pk_mul_f32 v[150:151], v[150:151], v[156:157] op_sel_hi:[1,0]
	v_pk_fma_f32 v[152:153], v[2:3], v[152:153], v[6:7]
	v_pk_fma_f32 v[150:151], v[4:5], v[150:151], v[8:9]
	v_cvt_pk_bf16_f32 v152, v152, v153
	v_cvt_pk_bf16_f32 v153, v150, v151
	global_store_dwordx2 v[146:147], v[152:153], off offset:1536
	ds_write2st64_b64 v157, v[148:149], v[152:153] offset0:42 offset1:43
	v_lshlrev_b32_e32 v152, 16, v135
	v_and_b32_e32 v153, 0xffff0000, v135
	v_lshlrev_b32_e32 v154, 16, v137
	v_and_b32_e32 v155, 0xffff0000, v137
	v_pk_fma_f32 v[152:153], v[152:153], s[2:3], v[154:155] op_sel_hi:[1,0,1]
	v_lshlrev_b32_e32 v154, 16, v134
	v_and_b32_e32 v155, 0xffff0000, v134
	v_lshlrev_b32_e32 v134, 16, v136
	v_and_b32_e32 v135, 0xffff0000, v136
	global_store_dwordx2 v[146:147], v[158:159], off offset:512
	global_store_dwordx2 v[146:147], v[148:149], off offset:1024
	v_lshlrev_b32_e32 v146, 16, v142
	v_and_b32_e32 v147, 0xffff0000, v142
	v_lshlrev_b32_e32 v148, 16, v144
	v_and_b32_e32 v149, 0xffff0000, v144
	v_and_b32_e32 v142, 0xffff0000, v143
	v_lshlrev_b32_e32 v143, 16, v143
	v_and_b32_e32 v144, 0xffff0000, v145
	v_lshlrev_b32_e32 v145, 16, v145
	v_pk_fma_f32 v[134:135], v[154:155], s[2:3], v[134:135] op_sel_hi:[1,0,1]
	v_pk_fma_f32 v[146:147], v[146:147], s[2:3], v[148:149] op_sel_hi:[1,0,1]
	v_pk_fma_f32 v[142:143], v[142:143], s[2:3], v[144:145] op_sel_hi:[1,0,1]
	v_lshlrev_b32_e32 v144, 16, v138
	v_and_b32_e32 v138, 0xffff0000, v138
	v_mov_b32_e32 v136, v134
	v_mov_b32_e32 v137, v153
	v_pk_mov_b32 v[154:155], v[134:135], v[152:153] op_sel:[1,0]
	v_lshlrev_b32_e32 v145, 16, v140
	v_mul_f32_e32 v138, 0x3fd744fd, v138
	v_and_b32_e32 v140, 0xffff0000, v140
	v_pk_add_f32 v[136:137], v[136:137], v[154:155]
	v_pk_add_f32 v[154:155], v[146:147], v[146:147] op_sel:[0,1] op_sel_hi:[1,0]
	v_pk_add_f32 v[156:157], v[142:143], v[142:143] op_sel:[0,1] op_sel_hi:[1,0]
	v_mov_b32_e32 v155, v138
	v_mov_b32_e32 v157, v140
	v_pk_add_f32 v[154:155], v[154:155], v[156:157]
	v_lshlrev_b32_e32 v156, 16, v131
	v_and_b32_e32 v157, 0xffff0000, v131
	v_lshlrev_b32_e32 v158, 16, v133
	v_and_b32_e32 v159, 0xffff0000, v133
	v_lshlrev_b32_e32 v148, 16, v139
	v_pk_fma_f32 v[156:157], v[156:157], s[2:3], v[158:159] op_sel_hi:[1,0,1]
	v_mul_f32_e32 v149, 0x3fd744fd, v148
	v_lshlrev_b32_e32 v151, 16, v141
	v_mov_b32_e32 v148, v157
	v_mov_b32_e32 v150, v156
	v_pk_add_f32 v[148:149], v[148:149], v[150:151]
	v_lshlrev_b32_e32 v150, 16, v130
	v_and_b32_e32 v151, 0xffff0000, v130
	v_lshlrev_b32_e32 v130, 16, v132
	v_and_b32_e32 v131, 0xffff0000, v132
	v_mul_f32_e32 v144, 0x3fd744fd, v144
	v_and_b32_e32 v139, 0xffff0000, v139
	v_pk_add_f32 v[136:137], v[136:137], v[136:137] op_sel:[0,1] op_sel_hi:[1,0]
	v_pk_fma_f32 v[130:131], v[150:151], s[2:3], v[130:131] op_sel_hi:[1,0,1]
	v_mul_f32_e32 v139, 0x3fd744fd, v139
	v_and_b32_e32 v141, 0xffff0000, v141
	v_mov_b32_e32 v137, v144
	v_mov_b32_e32 v144, v1
	v_mov_b32_e32 v138, v130
	v_mov_b32_e32 v140, v131
	v_pk_add_f32 v[136:137], v[136:137], v[144:145]
	v_pk_add_f32 v[132:133], v[138:139], v[140:141]
	v_pk_add_f32 v[144:145], v[136:137], v[154:155]
	v_pk_add_f32 v[138:139], v[132:133], v[148:149]
	v_mov_b32_e32 v154, v137
	v_pk_add_f32 v[138:139], v[144:145], v[138:139]
	s_nop 0
	v_add_f32_e32 v132, v138, v139
	s_nop 1
	v_add_f32_dpp v132, v132, v132 quad_perm:[1,0,3,2] row_mask:0xf bank_mask:0xf bound_ctrl:1
	s_nop 1
	v_add_f32_dpp v132, v132, v132 quad_perm:[2,3,0,1] row_mask:0xf bank_mask:0xf bound_ctrl:1
	s_nop 1
	v_add_f32_dpp v132, v132, v132 row_half_mirror row_mask:0xf bank_mask:0xf bound_ctrl:1
	s_nop 1
	v_add_f32_dpp v132, v132, v132 row_mirror row_mask:0xf bank_mask:0xf bound_ctrl:1
	v_mov_b32_e32 v136, v132
	s_nop 1
	v_permlane32_swap_b32 v132, v136
	s_nop 0
	v_add_f32_e32 v132, v132, v136
	v_mov_b32_e32 v136, v132
	s_nop 1
	v_permlane16_swap_b32_e32 v132, v136
	s_waitcnt lgkmcnt(0)
	v_add_f32_e32 v132, v132, v136
	v_mul_f32_e32 v136, 0x3a800000, v132
	v_pk_add_f32 v[134:135], v[134:135], v[136:137] op_sel_hi:[1,0] neg_lo:[0,1] neg_hi:[0,1]
	v_pk_add_f32 v[140:141], v[152:153], v[136:137] op_sel_hi:[1,0] neg_lo:[0,1] neg_hi:[0,1]
	v_pk_mul_f32 v[138:139], v[134:135], v[134:135]
	v_pk_mul_f32 v[144:145], v[140:141], v[140:141]
	v_add_f32_e32 v138, v138, v139
	v_pk_add_f32 v[146:147], v[146:147], v[136:137] op_sel_hi:[1,0] neg_lo:[0,1] neg_hi:[0,1]
	v_add_f32_e32 v138, v144, v138
	v_pk_mul_f32 v[160:161], v[146:147], v[146:147]
	v_add_f32_e32 v138, v145, v138
	v_pk_add_f32 v[142:143], v[142:143], v[136:137] op_sel_hi:[1,0] neg_lo:[0,1] neg_hi:[0,1]
	v_add_f32_e32 v138, v160, v138
	v_pk_mul_f32 v[158:159], v[142:143], v[142:143]
	v_add_f32_e32 v138, v161, v138
	v_pk_add_f32 v[130:131], v[130:131], v[136:137] op_sel_hi:[1,0] neg_lo:[0,1] neg_hi:[0,1]
	v_add_f32_e32 v138, v159, v138
	v_pk_mul_f32 v[150:151], v[130:131], v[130:131]
	v_add_f32_e32 v138, v158, v138
	v_pk_add_f32 v[152:153], v[156:157], v[136:137] op_sel_hi:[1,0] neg_lo:[0,1] neg_hi:[0,1]
	v_add_f32_e32 v138, v150, v138
	v_pk_mul_f32 v[156:157], v[152:153], v[152:153]
	v_mov_b32_e32 v132, v149
	v_add_f32_e32 v138, v151, v138
	v_pk_add_f32 v[132:133], v[132:133], v[136:137] op_sel_hi:[1,0] neg_lo:[0,1] neg_hi:[0,1]
	v_pk_add_f32 v[136:137], v[154:155], v[136:137] op_sel_hi:[1,0] neg_lo:[0,1] neg_hi:[0,1]
	v_add_f32_e32 v138, v156, v138
	v_pk_mul_f32 v[154:155], v[136:137], v[136:137]
	v_add_f32_e32 v138, v157, v138
	v_add_f32_e32 v138, v154, v138
	v_pk_mul_f32 v[148:149], v[132:133], v[132:133]
	v_add_f32_e32 v138, v155, v138
	v_add_f32_e32 v138, v148, v138
	v_add_f32_e32 v138, v149, v138
	s_nop 1
	v_add_f32_dpp v138, v138, v138 quad_perm:[1,0,3,2] row_mask:0xf bank_mask:0xf bound_ctrl:1
	s_nop 1
	v_add_f32_dpp v138, v138, v138 quad_perm:[2,3,0,1] row_mask:0xf bank_mask:0xf bound_ctrl:1
	s_nop 1
	v_add_f32_dpp v138, v138, v138 row_half_mirror row_mask:0xf bank_mask:0xf bound_ctrl:1
	s_nop 1
	v_add_f32_dpp v138, v138, v138 row_mirror row_mask:0xf bank_mask:0xf bound_ctrl:1
	v_mov_b32_e32 v139, v138
	s_nop 1
	v_permlane32_swap_b32 v138, v139
	s_nop 0
	v_add_f32_e32 v138, v138, v139
	v_mov_b32_e32 v139, v138
	s_nop 1
	v_permlane16_swap_b32_e32 v138, v139
	s_waitcnt lgkmcnt(0)
	v_add_f32_e32 v138, v138, v139
	v_fmamk_f32 v138, v138, 0x3a800000, v206
	v_mul_f32_e32 v139, 0x4f800000, v138
	v_cmp_gt_f32_e32 vcc, s45, v138
	s_nop 1
	v_cndmask_b32_e32 v138, v138, v139, vcc
	v_sqrt_f32_e32 v139, v138
	s_nop 0
	v_add_u32_e32 v144, -1, v139
	v_fma_f32 v145, -v144, v139, v138
	v_cmp_ge_f32_e64 s[0:1], 0, v145
	v_add_u32_e32 v145, 1, v139
	s_nop 0
	v_cndmask_b32_e64 v144, v139, v144, s[0:1]
	v_fma_f32 v139, -v145, v139, v138
	v_cmp_lt_f32_e64 s[0:1], 0, v139
	s_nop 1
	v_cndmask_b32_e64 v139, v144, v145, s[0:1]
	v_mul_f32_e32 v144, 0x37800000, v139
	v_cndmask_b32_e32 v139, v139, v144, vcc
	v_cmp_class_f32_e32 vcc, v138, v207
	s_nop 1
	v_cndmask_b32_e32 v138, v139, v138, vcc
	v_div_scale_f32 v139, s[0:1], v138, v138, 1.0
	v_rcp_f32_e32 v144, v139
	s_nop 0
	v_fma_f32 v145, -v139, v144, 1.0
	v_fmac_f32_e32 v144, v145, v144
	v_div_scale_f32 v145, vcc, 1.0, v138, 1.0
	v_mul_f32_e32 v148, v145, v144
	v_fma_f32 v149, -v139, v148, v145
	v_fmac_f32_e32 v148, v149, v144
	v_fma_f32 v139, -v139, v148, v145
	v_div_fmas_f32 v139, v139, v144, v148
	v_div_fixup_f32 v138, v139, v138, 1.0
	v_pk_mul_f32 v[134:135], v[134:135], v[138:139] op_sel_hi:[1,0]
	v_pk_mul_f32 v[140:141], v[140:141], v[138:139] op_sel_hi:[1,0]
	v_pk_fma_f32 v[134:135], v[26:27], v[134:135], v[30:31]
	v_pk_fma_f32 v[140:141], v[28:29], v[140:141], v[32:33]
	v_cvt_pk_bf16_f32 v134, v134, v135
	v_cvt_pk_bf16_f32 v135, v140, v141
	v_pk_mul_f32 v[140:141], v[146:147], v[138:139] op_sel_hi:[1,0]
	v_pk_mul_f32 v[142:143], v[142:143], v[138:139] op_sel_hi:[1,0]
	v_pk_fma_f32 v[140:141], v[18:19], v[140:141], v[22:23]
	v_pk_fma_f32 v[142:143], v[20:21], v[142:143], v[24:25] op_sel:[0,1,0] op_sel_hi:[1,0,1]
	v_cvt_pk_bf16_f32 v140, v140, v141
	v_cvt_pk_bf16_f32 v141, v142, v143
	v_add_u32_e32 v139, 48, v195
	global_store_dwordx2 v[128:129], v[134:135], off
	ds_write2st64_b64 v139, v[134:135], v[140:141] offset0:44 offset1:45
	v_pk_mul_f32 v[130:131], v[130:131], v[138:139] op_sel_hi:[1,0]
	v_pk_mul_f32 v[134:135], v[152:153], v[138:139] op_sel_hi:[1,0]
	v_pk_fma_f32 v[130:131], v[10:11], v[130:131], v[14:15]
	v_pk_fma_f32 v[134:135], v[12:13], v[134:135], v[16:17]
	v_cvt_pk_bf16_f32 v130, v130, v131
	v_cvt_pk_bf16_f32 v131, v134, v135
	v_pk_mul_f32 v[134:135], v[136:137], v[138:139] op_sel_hi:[1,0]
	v_pk_mul_f32 v[132:133], v[132:133], v[138:139] op_sel_hi:[1,0]
	v_pk_fma_f32 v[134:135], v[2:3], v[134:135], v[6:7]
	v_pk_fma_f32 v[132:133], v[4:5], v[132:133], v[8:9]
	v_cvt_pk_bf16_f32 v134, v134, v135
	v_cvt_pk_bf16_f32 v135, v132, v133
	global_store_dwordx2 v[128:129], v[134:135], off offset:1536
	ds_write2st64_b64 v139, v[130:131], v[134:135] offset0:46 offset1:47
	v_lshlrev_b32_e32 v134, 16, v117
	v_and_b32_e32 v135, 0xffff0000, v117
	v_lshlrev_b32_e32 v136, 16, v119
	v_and_b32_e32 v137, 0xffff0000, v119
	v_pk_fma_f32 v[134:135], v[134:135], s[2:3], v[136:137] op_sel_hi:[1,0,1]
	v_lshlrev_b32_e32 v136, 16, v116
	v_and_b32_e32 v137, 0xffff0000, v116
	v_lshlrev_b32_e32 v116, 16, v118
	v_and_b32_e32 v117, 0xffff0000, v118
	global_store_dwordx2 v[128:129], v[140:141], off offset:512
	global_store_dwordx2 v[128:129], v[130:131], off offset:1024
	v_lshlrev_b32_e32 v128, 16, v124
	v_and_b32_e32 v129, 0xffff0000, v124
	v_lshlrev_b32_e32 v130, 16, v126
	v_and_b32_e32 v131, 0xffff0000, v126
	v_and_b32_e32 v124, 0xffff0000, v125
	v_lshlrev_b32_e32 v125, 16, v125
	v_and_b32_e32 v126, 0xffff0000, v127
	v_lshlrev_b32_e32 v127, 16, v127
	v_pk_fma_f32 v[116:117], v[136:137], s[2:3], v[116:117] op_sel_hi:[1,0,1]
	v_pk_fma_f32 v[128:129], v[128:129], s[2:3], v[130:131] op_sel_hi:[1,0,1]
	v_pk_fma_f32 v[124:125], v[124:125], s[2:3], v[126:127] op_sel_hi:[1,0,1]
	v_lshlrev_b32_e32 v126, 16, v120
	v_and_b32_e32 v120, 0xffff0000, v120
	v_mov_b32_e32 v118, v116
	v_mov_b32_e32 v119, v135
	v_pk_mov_b32 v[136:137], v[116:117], v[134:135] op_sel:[1,0]
	v_lshlrev_b32_e32 v127, 16, v122
	v_mul_f32_e32 v120, 0x3fd744fd, v120
	v_and_b32_e32 v122, 0xffff0000, v122
	v_pk_add_f32 v[118:119], v[118:119], v[136:137]
	v_pk_add_f32 v[136:137], v[128:129], v[128:129] op_sel:[0,1] op_sel_hi:[1,0]
	v_pk_add_f32 v[138:139], v[124:125], v[124:125] op_sel:[0,1] op_sel_hi:[1,0]
	v_mov_b32_e32 v137, v120
	v_mov_b32_e32 v139, v122
	v_pk_add_f32 v[136:137], v[136:137], v[138:139]
	v_lshlrev_b32_e32 v138, 16, v113
	v_and_b32_e32 v139, 0xffff0000, v113
	v_lshlrev_b32_e32 v140, 16, v115
	v_and_b32_e32 v141, 0xffff0000, v115
	v_lshlrev_b32_e32 v130, 16, v121
	v_pk_fma_f32 v[138:139], v[138:139], s[2:3], v[140:141] op_sel_hi:[1,0,1]
	v_mul_f32_e32 v131, 0x3fd744fd, v130
	v_lshlrev_b32_e32 v133, 16, v123
	v_mov_b32_e32 v130, v139
	v_mov_b32_e32 v132, v138
	v_pk_add_f32 v[130:131], v[130:131], v[132:133]
	v_lshlrev_b32_e32 v132, 16, v112
	v_and_b32_e32 v133, 0xffff0000, v112
	v_lshlrev_b32_e32 v112, 16, v114
	v_and_b32_e32 v113, 0xffff0000, v114
	v_mul_f32_e32 v126, 0x3fd744fd, v126
	v_and_b32_e32 v121, 0xffff0000, v121
	v_pk_add_f32 v[118:119], v[118:119], v[118:119] op_sel:[0,1] op_sel_hi:[1,0]
	v_pk_fma_f32 v[112:113], v[132:133], s[2:3], v[112:113] op_sel_hi:[1,0,1]
	v_mul_f32_e32 v121, 0x3fd744fd, v121
	v_and_b32_e32 v123, 0xffff0000, v123
	v_mov_b32_e32 v119, v126
	v_mov_b32_e32 v126, v1
	v_mov_b32_e32 v120, v112
	v_mov_b32_e32 v122, v113
	v_pk_add_f32 v[118:119], v[118:119], v[126:127]
	v_pk_add_f32 v[114:115], v[120:121], v[122:123]
	v_pk_add_f32 v[126:127], v[118:119], v[136:137]
	v_pk_add_f32 v[120:121], v[114:115], v[130:131]
	v_mov_b32_e32 v136, v119
	v_pk_add_f32 v[120:121], v[126:127], v[120:121]
	s_nop 0
	v_add_f32_e32 v114, v120, v121
	s_nop 1
	v_add_f32_dpp v114, v114, v114 quad_perm:[1,0,3,2] row_mask:0xf bank_mask:0xf bound_ctrl:1
	s_nop 1
	v_add_f32_dpp v114, v114, v114 quad_perm:[2,3,0,1] row_mask:0xf bank_mask:0xf bound_ctrl:1
	s_nop 1
	v_add_f32_dpp v114, v114, v114 row_half_mirror row_mask:0xf bank_mask:0xf bound_ctrl:1
	s_nop 1
	v_add_f32_dpp v114, v114, v114 row_mirror row_mask:0xf bank_mask:0xf bound_ctrl:1
	v_mov_b32_e32 v118, v114
	s_nop 1
	v_permlane32_swap_b32 v114, v118
	s_nop 0
	v_add_f32_e32 v114, v114, v118
	v_mov_b32_e32 v118, v114
	s_nop 1
	v_permlane16_swap_b32_e32 v114, v118
	s_waitcnt lgkmcnt(0)
	v_add_f32_e32 v114, v114, v118
	v_mul_f32_e32 v118, 0x3a800000, v114
	v_pk_add_f32 v[116:117], v[116:117], v[118:119] op_sel_hi:[1,0] neg_lo:[0,1] neg_hi:[0,1]
	v_pk_add_f32 v[122:123], v[134:135], v[118:119] op_sel_hi:[1,0] neg_lo:[0,1] neg_hi:[0,1]
	v_pk_mul_f32 v[120:121], v[116:117], v[116:117]
	v_pk_mul_f32 v[126:127], v[122:123], v[122:123]
	v_add_f32_e32 v120, v120, v121
	v_pk_add_f32 v[128:129], v[128:129], v[118:119] op_sel_hi:[1,0] neg_lo:[0,1] neg_hi:[0,1]
	v_add_f32_e32 v120, v126, v120
	v_pk_mul_f32 v[142:143], v[128:129], v[128:129]
	v_add_f32_e32 v120, v127, v120
	v_pk_add_f32 v[124:125], v[124:125], v[118:119] op_sel_hi:[1,0] neg_lo:[0,1] neg_hi:[0,1]
	v_add_f32_e32 v120, v142, v120
	v_pk_mul_f32 v[140:141], v[124:125], v[124:125]
	v_add_f32_e32 v120, v143, v120
	v_pk_add_f32 v[112:113], v[112:113], v[118:119] op_sel_hi:[1,0] neg_lo:[0,1] neg_hi:[0,1]
	v_add_f32_e32 v120, v141, v120
	v_pk_mul_f32 v[132:133], v[112:113], v[112:113]
	v_add_f32_e32 v120, v140, v120
	v_pk_add_f32 v[134:135], v[138:139], v[118:119] op_sel_hi:[1,0] neg_lo:[0,1] neg_hi:[0,1]
	v_add_f32_e32 v120, v132, v120
	v_pk_mul_f32 v[138:139], v[134:135], v[134:135]
	v_mov_b32_e32 v114, v131
	v_add_f32_e32 v120, v133, v120
	v_pk_add_f32 v[114:115], v[114:115], v[118:119] op_sel_hi:[1,0] neg_lo:[0,1] neg_hi:[0,1]
	v_pk_add_f32 v[118:119], v[136:137], v[118:119] op_sel_hi:[1,0] neg_lo:[0,1] neg_hi:[0,1]
	v_add_f32_e32 v120, v138, v120
	v_pk_mul_f32 v[136:137], v[118:119], v[118:119]
	v_add_f32_e32 v120, v139, v120
	v_add_f32_e32 v120, v136, v120
	v_pk_mul_f32 v[130:131], v[114:115], v[114:115]
	v_add_f32_e32 v120, v137, v120
	v_add_f32_e32 v120, v130, v120
	v_add_f32_e32 v120, v131, v120
	s_nop 1
	v_add_f32_dpp v120, v120, v120 quad_perm:[1,0,3,2] row_mask:0xf bank_mask:0xf bound_ctrl:1
	s_nop 1
	v_add_f32_dpp v120, v120, v120 quad_perm:[2,3,0,1] row_mask:0xf bank_mask:0xf bound_ctrl:1
	s_nop 1
	v_add_f32_dpp v120, v120, v120 row_half_mirror row_mask:0xf bank_mask:0xf bound_ctrl:1
	s_nop 1
	v_add_f32_dpp v120, v120, v120 row_mirror row_mask:0xf bank_mask:0xf bound_ctrl:1
	v_mov_b32_e32 v121, v120
	s_nop 1
	v_permlane32_swap_b32 v120, v121
	s_nop 0
	v_add_f32_e32 v120, v120, v121
	v_mov_b32_e32 v121, v120
	s_nop 1
	v_permlane16_swap_b32_e32 v120, v121
	s_waitcnt lgkmcnt(0)
	v_add_f32_e32 v120, v120, v121
	v_fmamk_f32 v120, v120, 0x3a800000, v206
	v_mul_f32_e32 v121, 0x4f800000, v120
	v_cmp_gt_f32_e32 vcc, s45, v120
	s_nop 1
	v_cndmask_b32_e32 v120, v120, v121, vcc
	v_sqrt_f32_e32 v121, v120
	s_nop 0
	v_add_u32_e32 v126, -1, v121
	v_fma_f32 v127, -v126, v121, v120
	v_cmp_ge_f32_e64 s[0:1], 0, v127
	v_add_u32_e32 v127, 1, v121
	s_nop 0
	v_cndmask_b32_e64 v126, v121, v126, s[0:1]
	v_fma_f32 v121, -v127, v121, v120
	v_cmp_lt_f32_e64 s[0:1], 0, v121
	s_nop 1
	v_cndmask_b32_e64 v121, v126, v127, s[0:1]
	v_mul_f32_e32 v126, 0x37800000, v121
	v_cndmask_b32_e32 v121, v121, v126, vcc
	v_cmp_class_f32_e32 vcc, v120, v207
	s_nop 1
	v_cndmask_b32_e32 v120, v121, v120, vcc
	v_div_scale_f32 v121, s[0:1], v120, v120, 1.0
	v_rcp_f32_e32 v126, v121
	s_nop 0
	v_fma_f32 v127, -v121, v126, 1.0
	v_fmac_f32_e32 v126, v127, v126
	v_div_scale_f32 v127, vcc, 1.0, v120, 1.0
	v_mul_f32_e32 v130, v127, v126
	v_fma_f32 v131, -v121, v130, v127
	v_fmac_f32_e32 v130, v131, v126
	v_fma_f32 v121, -v121, v130, v127
	v_div_fmas_f32 v121, v121, v126, v130
	v_div_fixup_f32 v120, v121, v120, 1.0
	v_pk_mul_f32 v[116:117], v[116:117], v[120:121] op_sel_hi:[1,0]
	v_pk_mul_f32 v[122:123], v[122:123], v[120:121] op_sel_hi:[1,0]
	v_pk_fma_f32 v[116:117], v[26:27], v[116:117], v[30:31]
	v_pk_fma_f32 v[122:123], v[28:29], v[122:123], v[32:33]
	v_cvt_pk_bf16_f32 v116, v116, v117
	v_cvt_pk_bf16_f32 v117, v122, v123
	v_pk_mul_f32 v[122:123], v[128:129], v[120:121] op_sel_hi:[1,0]
	v_pk_mul_f32 v[124:125], v[124:125], v[120:121] op_sel_hi:[1,0]
	v_pk_fma_f32 v[122:123], v[18:19], v[122:123], v[22:23]
	v_pk_fma_f32 v[124:125], v[20:21], v[124:125], v[24:25] op_sel:[0,1,0] op_sel_hi:[1,0,1]
	v_cvt_pk_bf16_f32 v122, v122, v123
	v_cvt_pk_bf16_f32 v123, v124, v125
	v_add_u32_e32 v121, 64, v195
	global_store_dwordx2 v[110:111], v[116:117], off
	ds_write2st64_b64 v121, v[116:117], v[122:123] offset0:48 offset1:49
	v_pk_mul_f32 v[112:113], v[112:113], v[120:121] op_sel_hi:[1,0]
	v_pk_mul_f32 v[116:117], v[134:135], v[120:121] op_sel_hi:[1,0]
	v_pk_fma_f32 v[112:113], v[10:11], v[112:113], v[14:15]
	v_pk_fma_f32 v[116:117], v[12:13], v[116:117], v[16:17]
	v_cvt_pk_bf16_f32 v112, v112, v113
	v_cvt_pk_bf16_f32 v113, v116, v117
	v_pk_mul_f32 v[116:117], v[118:119], v[120:121] op_sel_hi:[1,0]
	v_pk_mul_f32 v[114:115], v[114:115], v[120:121] op_sel_hi:[1,0]
	v_pk_fma_f32 v[116:117], v[2:3], v[116:117], v[6:7]
	v_pk_fma_f32 v[114:115], v[4:5], v[114:115], v[8:9]
	v_cvt_pk_bf16_f32 v116, v116, v117
	v_cvt_pk_bf16_f32 v117, v114, v115
	global_store_dwordx2 v[110:111], v[116:117], off offset:1536
	ds_write2st64_b64 v121, v[112:113], v[116:117] offset0:50 offset1:51
	v_lshlrev_b32_e32 v116, 16, v99
	v_and_b32_e32 v117, 0xffff0000, v99
	v_lshlrev_b32_e32 v118, 16, v101
	v_and_b32_e32 v119, 0xffff0000, v101
	v_pk_fma_f32 v[116:117], v[116:117], s[2:3], v[118:119] op_sel_hi:[1,0,1]
	v_lshlrev_b32_e32 v118, 16, v98
	v_and_b32_e32 v119, 0xffff0000, v98
	v_lshlrev_b32_e32 v98, 16, v100
	v_and_b32_e32 v99, 0xffff0000, v100
	global_store_dwordx2 v[110:111], v[122:123], off offset:512
	global_store_dwordx2 v[110:111], v[112:113], off offset:1024
	v_lshlrev_b32_e32 v110, 16, v106
	v_and_b32_e32 v111, 0xffff0000, v106
	v_lshlrev_b32_e32 v112, 16, v108
	v_and_b32_e32 v113, 0xffff0000, v108
	v_and_b32_e32 v106, 0xffff0000, v107
	v_lshlrev_b32_e32 v107, 16, v107
	v_and_b32_e32 v108, 0xffff0000, v109
	v_lshlrev_b32_e32 v109, 16, v109
	v_pk_fma_f32 v[98:99], v[118:119], s[2:3], v[98:99] op_sel_hi:[1,0,1]
	v_pk_fma_f32 v[110:111], v[110:111], s[2:3], v[112:113] op_sel_hi:[1,0,1]
	v_pk_fma_f32 v[106:107], v[106:107], s[2:3], v[108:109] op_sel_hi:[1,0,1]
	v_lshlrev_b32_e32 v108, 16, v102
	v_and_b32_e32 v102, 0xffff0000, v102
	v_mov_b32_e32 v100, v98
	v_mov_b32_e32 v101, v117
	v_pk_mov_b32 v[118:119], v[98:99], v[116:117] op_sel:[1,0]
	v_lshlrev_b32_e32 v109, 16, v104
	v_mul_f32_e32 v102, 0x3fd744fd, v102
	v_and_b32_e32 v104, 0xffff0000, v104
	v_pk_add_f32 v[100:101], v[100:101], v[118:119]
	v_pk_add_f32 v[118:119], v[110:111], v[110:111] op_sel:[0,1] op_sel_hi:[1,0]
	v_pk_add_f32 v[120:121], v[106:107], v[106:107] op_sel:[0,1] op_sel_hi:[1,0]
	v_mov_b32_e32 v119, v102
	v_mov_b32_e32 v121, v104
	v_pk_add_f32 v[118:119], v[118:119], v[120:121]
	v_lshlrev_b32_e32 v120, 16, v95
	v_and_b32_e32 v121, 0xffff0000, v95
	v_lshlrev_b32_e32 v122, 16, v97
	v_and_b32_e32 v123, 0xffff0000, v97
	v_lshlrev_b32_e32 v112, 16, v103
	v_pk_fma_f32 v[120:121], v[120:121], s[2:3], v[122:123] op_sel_hi:[1,0,1]
	v_mul_f32_e32 v113, 0x3fd744fd, v112
	v_lshlrev_b32_e32 v115, 16, v105
	v_mov_b32_e32 v112, v121
	v_mov_b32_e32 v114, v120
	v_pk_add_f32 v[112:113], v[112:113], v[114:115]
	v_lshlrev_b32_e32 v114, 16, v94
	v_and_b32_e32 v115, 0xffff0000, v94
	v_lshlrev_b32_e32 v94, 16, v96
	v_and_b32_e32 v95, 0xffff0000, v96
	v_mul_f32_e32 v108, 0x3fd744fd, v108
	v_and_b32_e32 v103, 0xffff0000, v103
	v_pk_add_f32 v[100:101], v[100:101], v[100:101] op_sel:[0,1] op_sel_hi:[1,0]
	v_pk_fma_f32 v[94:95], v[114:115], s[2:3], v[94:95] op_sel_hi:[1,0,1]
	v_mul_f32_e32 v103, 0x3fd744fd, v103
	v_and_b32_e32 v105, 0xffff0000, v105
	v_mov_b32_e32 v101, v108
	v_mov_b32_e32 v108, v1
	v_mov_b32_e32 v102, v94
	v_mov_b32_e32 v104, v95
	v_pk_add_f32 v[100:101], v[100:101], v[108:109]
	v_pk_add_f32 v[96:97], v[102:103], v[104:105]
	v_pk_add_f32 v[108:109], v[100:101], v[118:119]
	v_pk_add_f32 v[102:103], v[96:97], v[112:113]
	v_mov_b32_e32 v118, v101
	v_pk_add_f32 v[102:103], v[108:109], v[102:103]
	s_nop 0
	v_add_f32_e32 v96, v102, v103
	s_nop 1
	v_add_f32_dpp v96, v96, v96 quad_perm:[1,0,3,2] row_mask:0xf bank_mask:0xf bound_ctrl:1
	s_nop 1
	v_add_f32_dpp v96, v96, v96 quad_perm:[2,3,0,1] row_mask:0xf bank_mask:0xf bound_ctrl:1
	s_nop 1
	v_add_f32_dpp v96, v96, v96 row_half_mirror row_mask:0xf bank_mask:0xf bound_ctrl:1
	s_nop 1
	v_add_f32_dpp v96, v96, v96 row_mirror row_mask:0xf bank_mask:0xf bound_ctrl:1
	v_mov_b32_e32 v100, v96
	s_nop 1
	v_permlane32_swap_b32 v96, v100
	s_nop 0
	v_add_f32_e32 v96, v96, v100
	v_mov_b32_e32 v100, v96
	s_nop 1
	v_permlane16_swap_b32_e32 v96, v100
	s_waitcnt lgkmcnt(0)
	v_add_f32_e32 v96, v96, v100
	v_mul_f32_e32 v100, 0x3a800000, v96
	v_pk_add_f32 v[98:99], v[98:99], v[100:101] op_sel_hi:[1,0] neg_lo:[0,1] neg_hi:[0,1]
	v_pk_add_f32 v[104:105], v[116:117], v[100:101] op_sel_hi:[1,0] neg_lo:[0,1] neg_hi:[0,1]
	v_pk_mul_f32 v[102:103], v[98:99], v[98:99]
	v_pk_mul_f32 v[108:109], v[104:105], v[104:105]
	v_add_f32_e32 v102, v102, v103
	v_pk_add_f32 v[110:111], v[110:111], v[100:101] op_sel_hi:[1,0] neg_lo:[0,1] neg_hi:[0,1]
	v_add_f32_e32 v102, v108, v102
	v_pk_mul_f32 v[124:125], v[110:111], v[110:111]
	v_add_f32_e32 v102, v109, v102
	v_pk_add_f32 v[106:107], v[106:107], v[100:101] op_sel_hi:[1,0] neg_lo:[0,1] neg_hi:[0,1]
	v_add_f32_e32 v102, v124, v102
	v_pk_mul_f32 v[122:123], v[106:107], v[106:107]
	v_add_f32_e32 v102, v125, v102
	v_pk_add_f32 v[94:95], v[94:95], v[100:101] op_sel_hi:[1,0] neg_lo:[0,1] neg_hi:[0,1]
	v_add_f32_e32 v102, v123, v102
	v_pk_mul_f32 v[114:115], v[94:95], v[94:95]
	v_add_f32_e32 v102, v122, v102
	v_pk_add_f32 v[116:117], v[120:121], v[100:101] op_sel_hi:[1,0] neg_lo:[0,1] neg_hi:[0,1]
	v_add_f32_e32 v102, v114, v102
	v_pk_mul_f32 v[120:121], v[116:117], v[116:117]
	v_mov_b32_e32 v96, v113
	v_add_f32_e32 v102, v115, v102
	v_pk_add_f32 v[96:97], v[96:97], v[100:101] op_sel_hi:[1,0] neg_lo:[0,1] neg_hi:[0,1]
	v_pk_add_f32 v[100:101], v[118:119], v[100:101] op_sel_hi:[1,0] neg_lo:[0,1] neg_hi:[0,1]
	v_add_f32_e32 v102, v120, v102
	v_pk_mul_f32 v[118:119], v[100:101], v[100:101]
	v_add_f32_e32 v102, v121, v102
	v_add_f32_e32 v102, v118, v102
	v_pk_mul_f32 v[112:113], v[96:97], v[96:97]
	v_add_f32_e32 v102, v119, v102
	v_add_f32_e32 v102, v112, v102
	v_add_f32_e32 v102, v113, v102
	s_nop 1
	v_add_f32_dpp v102, v102, v102 quad_perm:[1,0,3,2] row_mask:0xf bank_mask:0xf bound_ctrl:1
	s_nop 1
	v_add_f32_dpp v102, v102, v102 quad_perm:[2,3,0,1] row_mask:0xf bank_mask:0xf bound_ctrl:1
	s_nop 1
	v_add_f32_dpp v102, v102, v102 row_half_mirror row_mask:0xf bank_mask:0xf bound_ctrl:1
	s_nop 1
	v_add_f32_dpp v102, v102, v102 row_mirror row_mask:0xf bank_mask:0xf bound_ctrl:1
	v_mov_b32_e32 v103, v102
	s_nop 1
	v_permlane32_swap_b32 v102, v103
	s_nop 0
	v_add_f32_e32 v102, v102, v103
	v_mov_b32_e32 v103, v102
	s_nop 1
	v_permlane16_swap_b32_e32 v102, v103
	s_waitcnt lgkmcnt(0)
	v_add_f32_e32 v102, v102, v103
	v_fmamk_f32 v102, v102, 0x3a800000, v206
	v_mul_f32_e32 v103, 0x4f800000, v102
	v_cmp_gt_f32_e32 vcc, s45, v102
	s_nop 1
	v_cndmask_b32_e32 v102, v102, v103, vcc
	v_sqrt_f32_e32 v103, v102
	s_nop 0
	v_add_u32_e32 v108, -1, v103
	v_fma_f32 v109, -v108, v103, v102
	v_cmp_ge_f32_e64 s[0:1], 0, v109
	v_add_u32_e32 v109, 1, v103
	s_nop 0
	v_cndmask_b32_e64 v108, v103, v108, s[0:1]
	v_fma_f32 v103, -v109, v103, v102
	v_cmp_lt_f32_e64 s[0:1], 0, v103
	s_nop 1
	v_cndmask_b32_e64 v103, v108, v109, s[0:1]
	v_mul_f32_e32 v108, 0x37800000, v103
	v_cndmask_b32_e32 v103, v103, v108, vcc
	v_cmp_class_f32_e32 vcc, v102, v207
	s_nop 1
	v_cndmask_b32_e32 v102, v103, v102, vcc
	v_div_scale_f32 v103, s[0:1], v102, v102, 1.0
	v_rcp_f32_e32 v108, v103
	s_nop 0
	v_fma_f32 v109, -v103, v108, 1.0
	v_fmac_f32_e32 v108, v109, v108
	v_div_scale_f32 v109, vcc, 1.0, v102, 1.0
	v_mul_f32_e32 v112, v109, v108
	v_fma_f32 v113, -v103, v112, v109
	v_fmac_f32_e32 v112, v113, v108
	v_fma_f32 v103, -v103, v112, v109
	v_div_fmas_f32 v103, v103, v108, v112
	v_div_fixup_f32 v102, v103, v102, 1.0
	v_pk_mul_f32 v[98:99], v[98:99], v[102:103] op_sel_hi:[1,0]
	v_pk_mul_f32 v[104:105], v[104:105], v[102:103] op_sel_hi:[1,0]
	v_pk_fma_f32 v[98:99], v[26:27], v[98:99], v[30:31]
	v_pk_fma_f32 v[104:105], v[28:29], v[104:105], v[32:33]
	v_cvt_pk_bf16_f32 v98, v98, v99
	v_cvt_pk_bf16_f32 v99, v104, v105
	v_pk_mul_f32 v[104:105], v[110:111], v[102:103] op_sel_hi:[1,0]
	v_pk_mul_f32 v[106:107], v[106:107], v[102:103] op_sel_hi:[1,0]
	v_pk_fma_f32 v[104:105], v[18:19], v[104:105], v[22:23]
	v_pk_fma_f32 v[106:107], v[20:21], v[106:107], v[24:25] op_sel:[0,1,0] op_sel_hi:[1,0,1]
	v_cvt_pk_bf16_f32 v104, v104, v105
	v_cvt_pk_bf16_f32 v105, v106, v107
	v_add_u32_e32 v103, 0x50, v195
	global_store_dwordx2 v[92:93], v[98:99], off
	ds_write2st64_b64 v103, v[98:99], v[104:105] offset0:52 offset1:53
	v_pk_mul_f32 v[94:95], v[94:95], v[102:103] op_sel_hi:[1,0]
	v_pk_mul_f32 v[98:99], v[116:117], v[102:103] op_sel_hi:[1,0]
	v_pk_fma_f32 v[94:95], v[10:11], v[94:95], v[14:15]
	v_pk_fma_f32 v[98:99], v[12:13], v[98:99], v[16:17]
	v_cvt_pk_bf16_f32 v94, v94, v95
	v_cvt_pk_bf16_f32 v95, v98, v99
	v_pk_mul_f32 v[98:99], v[100:101], v[102:103] op_sel_hi:[1,0]
	v_pk_mul_f32 v[96:97], v[96:97], v[102:103] op_sel_hi:[1,0]
	v_pk_fma_f32 v[98:99], v[2:3], v[98:99], v[6:7]
	v_pk_fma_f32 v[96:97], v[4:5], v[96:97], v[8:9]
	v_cvt_pk_bf16_f32 v98, v98, v99
	v_cvt_pk_bf16_f32 v99, v96, v97
	global_store_dwordx2 v[92:93], v[98:99], off offset:1536
	ds_write2st64_b64 v103, v[94:95], v[98:99] offset0:54 offset1:55
	v_lshlrev_b32_e32 v98, 16, v81
	v_and_b32_e32 v99, 0xffff0000, v81
	v_lshlrev_b32_e32 v100, 16, v83
	v_and_b32_e32 v101, 0xffff0000, v83
	v_pk_fma_f32 v[98:99], v[98:99], s[2:3], v[100:101] op_sel_hi:[1,0,1]
	v_lshlrev_b32_e32 v100, 16, v80
	v_and_b32_e32 v101, 0xffff0000, v80
	v_lshlrev_b32_e32 v80, 16, v82
	v_and_b32_e32 v81, 0xffff0000, v82
	global_store_dwordx2 v[92:93], v[104:105], off offset:512
	global_store_dwordx2 v[92:93], v[94:95], off offset:1024
	v_lshlrev_b32_e32 v92, 16, v88
	v_and_b32_e32 v93, 0xffff0000, v88
	v_lshlrev_b32_e32 v94, 16, v90
	v_and_b32_e32 v95, 0xffff0000, v90
	v_and_b32_e32 v88, 0xffff0000, v89
	v_lshlrev_b32_e32 v89, 16, v89
	v_and_b32_e32 v90, 0xffff0000, v91
	v_lshlrev_b32_e32 v91, 16, v91
	v_pk_fma_f32 v[80:81], v[100:101], s[2:3], v[80:81] op_sel_hi:[1,0,1]
	v_pk_fma_f32 v[92:93], v[92:93], s[2:3], v[94:95] op_sel_hi:[1,0,1]
	v_pk_fma_f32 v[88:89], v[88:89], s[2:3], v[90:91] op_sel_hi:[1,0,1]
	v_lshlrev_b32_e32 v90, 16, v84
	v_and_b32_e32 v84, 0xffff0000, v84
	v_mov_b32_e32 v82, v80
	v_mov_b32_e32 v83, v99
	v_pk_mov_b32 v[100:101], v[80:81], v[98:99] op_sel:[1,0]
	v_lshlrev_b32_e32 v91, 16, v86
	v_mul_f32_e32 v84, 0x3fd744fd, v84
	v_and_b32_e32 v86, 0xffff0000, v86
	v_pk_add_f32 v[82:83], v[82:83], v[100:101]
	v_pk_add_f32 v[100:101], v[92:93], v[92:93] op_sel:[0,1] op_sel_hi:[1,0]
	v_pk_add_f32 v[102:103], v[88:89], v[88:89] op_sel:[0,1] op_sel_hi:[1,0]
	v_mov_b32_e32 v101, v84
	v_mov_b32_e32 v103, v86
	v_pk_add_f32 v[100:101], v[100:101], v[102:103]
	v_lshlrev_b32_e32 v102, 16, v77
	v_and_b32_e32 v103, 0xffff0000, v77
	v_lshlrev_b32_e32 v104, 16, v79
	v_and_b32_e32 v105, 0xffff0000, v79
	v_lshlrev_b32_e32 v94, 16, v85
	v_pk_fma_f32 v[102:103], v[102:103], s[2:3], v[104:105] op_sel_hi:[1,0,1]
	v_mul_f32_e32 v95, 0x3fd744fd, v94
	v_lshlrev_b32_e32 v97, 16, v87
	v_mov_b32_e32 v94, v103
	v_mov_b32_e32 v96, v102
	v_pk_add_f32 v[94:95], v[94:95], v[96:97]
	v_lshlrev_b32_e32 v96, 16, v76
	v_and_b32_e32 v97, 0xffff0000, v76
	v_lshlrev_b32_e32 v76, 16, v78
	v_and_b32_e32 v77, 0xffff0000, v78
	v_mul_f32_e32 v90, 0x3fd744fd, v90
	v_and_b32_e32 v85, 0xffff0000, v85
	v_pk_add_f32 v[82:83], v[82:83], v[82:83] op_sel:[0,1] op_sel_hi:[1,0]
	v_pk_fma_f32 v[76:77], v[96:97], s[2:3], v[76:77] op_sel_hi:[1,0,1]
	v_mul_f32_e32 v85, 0x3fd744fd, v85
	v_and_b32_e32 v87, 0xffff0000, v87
	v_mov_b32_e32 v83, v90
	v_mov_b32_e32 v90, v1
	v_mov_b32_e32 v84, v76
	v_mov_b32_e32 v86, v77
	v_pk_add_f32 v[82:83], v[82:83], v[90:91]
	v_pk_add_f32 v[78:79], v[84:85], v[86:87]
	v_pk_add_f32 v[90:91], v[82:83], v[100:101]
	v_pk_add_f32 v[84:85], v[78:79], v[94:95]
	v_mov_b32_e32 v100, v83
	v_pk_add_f32 v[84:85], v[90:91], v[84:85]
	s_nop 0
	v_add_f32_e32 v78, v84, v85
	s_nop 1
	v_add_f32_dpp v78, v78, v78 quad_perm:[1,0,3,2] row_mask:0xf bank_mask:0xf bound_ctrl:1
	s_nop 1
	v_add_f32_dpp v78, v78, v78 quad_perm:[2,3,0,1] row_mask:0xf bank_mask:0xf bound_ctrl:1
	s_nop 1
	v_add_f32_dpp v78, v78, v78 row_half_mirror row_mask:0xf bank_mask:0xf bound_ctrl:1
	s_nop 1
	v_add_f32_dpp v78, v78, v78 row_mirror row_mask:0xf bank_mask:0xf bound_ctrl:1
	v_mov_b32_e32 v82, v78
	s_nop 1
	v_permlane32_swap_b32 v78, v82
	s_nop 0
	v_add_f32_e32 v78, v78, v82
	v_mov_b32_e32 v82, v78
	s_nop 1
	v_permlane16_swap_b32_e32 v78, v82
	s_waitcnt lgkmcnt(0)
	v_add_f32_e32 v78, v78, v82
	v_mul_f32_e32 v82, 0x3a800000, v78
	v_pk_add_f32 v[80:81], v[80:81], v[82:83] op_sel_hi:[1,0] neg_lo:[0,1] neg_hi:[0,1]
	v_pk_add_f32 v[86:87], v[98:99], v[82:83] op_sel_hi:[1,0] neg_lo:[0,1] neg_hi:[0,1]
	v_pk_mul_f32 v[84:85], v[80:81], v[80:81]
	v_pk_mul_f32 v[90:91], v[86:87], v[86:87]
	v_add_f32_e32 v84, v84, v85
	v_pk_add_f32 v[92:93], v[92:93], v[82:83] op_sel_hi:[1,0] neg_lo:[0,1] neg_hi:[0,1]
	v_add_f32_e32 v84, v90, v84
	v_pk_mul_f32 v[106:107], v[92:93], v[92:93]
	v_add_f32_e32 v84, v91, v84
	v_pk_add_f32 v[88:89], v[88:89], v[82:83] op_sel_hi:[1,0] neg_lo:[0,1] neg_hi:[0,1]
	v_add_f32_e32 v84, v106, v84
	v_pk_mul_f32 v[104:105], v[88:89], v[88:89]
	v_add_f32_e32 v84, v107, v84
	v_pk_add_f32 v[76:77], v[76:77], v[82:83] op_sel_hi:[1,0] neg_lo:[0,1] neg_hi:[0,1]
	v_add_f32_e32 v84, v105, v84
	v_pk_mul_f32 v[96:97], v[76:77], v[76:77]
	v_add_f32_e32 v84, v104, v84
	v_pk_add_f32 v[98:99], v[102:103], v[82:83] op_sel_hi:[1,0] neg_lo:[0,1] neg_hi:[0,1]
	v_add_f32_e32 v84, v96, v84
	v_pk_mul_f32 v[102:103], v[98:99], v[98:99]
	v_mov_b32_e32 v78, v95
	v_add_f32_e32 v84, v97, v84
	v_pk_add_f32 v[78:79], v[78:79], v[82:83] op_sel_hi:[1,0] neg_lo:[0,1] neg_hi:[0,1]
	v_pk_add_f32 v[82:83], v[100:101], v[82:83] op_sel_hi:[1,0] neg_lo:[0,1] neg_hi:[0,1]
	v_add_f32_e32 v84, v102, v84
	v_pk_mul_f32 v[100:101], v[82:83], v[82:83]
	v_add_f32_e32 v84, v103, v84
	v_add_f32_e32 v84, v100, v84
	v_pk_mul_f32 v[94:95], v[78:79], v[78:79]
	v_add_f32_e32 v84, v101, v84
	v_add_f32_e32 v84, v94, v84
	v_add_f32_e32 v84, v95, v84
	s_nop 1
	v_add_f32_dpp v84, v84, v84 quad_perm:[1,0,3,2] row_mask:0xf bank_mask:0xf bound_ctrl:1
	s_nop 1
	v_add_f32_dpp v84, v84, v84 quad_perm:[2,3,0,1] row_mask:0xf bank_mask:0xf bound_ctrl:1
	s_nop 1
	v_add_f32_dpp v84, v84, v84 row_half_mirror row_mask:0xf bank_mask:0xf bound_ctrl:1
	s_nop 1
	v_add_f32_dpp v84, v84, v84 row_mirror row_mask:0xf bank_mask:0xf bound_ctrl:1
	v_mov_b32_e32 v85, v84
	s_nop 1
	v_permlane32_swap_b32 v84, v85
	s_nop 0
	v_add_f32_e32 v84, v84, v85
	v_mov_b32_e32 v85, v84
	s_nop 1
	v_permlane16_swap_b32_e32 v84, v85
	s_waitcnt lgkmcnt(0)
	v_add_f32_e32 v84, v84, v85
	v_fmamk_f32 v84, v84, 0x3a800000, v206
	v_mul_f32_e32 v85, 0x4f800000, v84
	v_cmp_gt_f32_e32 vcc, s45, v84
	s_nop 1
	v_cndmask_b32_e32 v84, v84, v85, vcc
	v_sqrt_f32_e32 v85, v84
	s_nop 0
	v_add_u32_e32 v90, -1, v85
	v_fma_f32 v91, -v90, v85, v84
	v_cmp_ge_f32_e64 s[0:1], 0, v91
	v_add_u32_e32 v91, 1, v85
	s_nop 0
	v_cndmask_b32_e64 v90, v85, v90, s[0:1]
	v_fma_f32 v85, -v91, v85, v84
	v_cmp_lt_f32_e64 s[0:1], 0, v85
	s_nop 1
	v_cndmask_b32_e64 v85, v90, v91, s[0:1]
	v_mul_f32_e32 v90, 0x37800000, v85
	v_cndmask_b32_e32 v85, v85, v90, vcc
	v_cmp_class_f32_e32 vcc, v84, v207
	s_nop 1
	v_cndmask_b32_e32 v84, v85, v84, vcc
	v_div_scale_f32 v85, s[0:1], v84, v84, 1.0
	v_rcp_f32_e32 v90, v85
	s_nop 0
	v_fma_f32 v91, -v85, v90, 1.0
	v_fmac_f32_e32 v90, v91, v90
	v_div_scale_f32 v91, vcc, 1.0, v84, 1.0
	v_mul_f32_e32 v94, v91, v90
	v_fma_f32 v95, -v85, v94, v91
	v_fmac_f32_e32 v94, v95, v90
	v_fma_f32 v85, -v85, v94, v91
	v_div_fmas_f32 v85, v85, v90, v94
	v_div_fixup_f32 v84, v85, v84, 1.0
	v_pk_mul_f32 v[80:81], v[80:81], v[84:85] op_sel_hi:[1,0]
	v_pk_mul_f32 v[86:87], v[86:87], v[84:85] op_sel_hi:[1,0]
	v_pk_fma_f32 v[80:81], v[26:27], v[80:81], v[30:31]
	v_pk_fma_f32 v[86:87], v[28:29], v[86:87], v[32:33]
	v_cvt_pk_bf16_f32 v80, v80, v81
	v_cvt_pk_bf16_f32 v81, v86, v87
	v_pk_mul_f32 v[86:87], v[92:93], v[84:85] op_sel_hi:[1,0]
	v_pk_mul_f32 v[88:89], v[88:89], v[84:85] op_sel_hi:[1,0]
	v_pk_fma_f32 v[86:87], v[18:19], v[86:87], v[22:23]
	v_pk_fma_f32 v[88:89], v[20:21], v[88:89], v[24:25] op_sel:[0,1,0] op_sel_hi:[1,0,1]
	v_cvt_pk_bf16_f32 v86, v86, v87
	v_cvt_pk_bf16_f32 v87, v88, v89
	v_add_u32_e32 v85, 0x60, v195
	global_store_dwordx2 v[74:75], v[80:81], off
	ds_write2st64_b64 v85, v[80:81], v[86:87] offset0:56 offset1:57
	v_pk_mul_f32 v[76:77], v[76:77], v[84:85] op_sel_hi:[1,0]
	v_pk_mul_f32 v[80:81], v[98:99], v[84:85] op_sel_hi:[1,0]
	v_pk_fma_f32 v[76:77], v[10:11], v[76:77], v[14:15]
	v_pk_fma_f32 v[80:81], v[12:13], v[80:81], v[16:17]
	v_cvt_pk_bf16_f32 v76, v76, v77
	v_cvt_pk_bf16_f32 v77, v80, v81
	v_pk_mul_f32 v[80:81], v[82:83], v[84:85] op_sel_hi:[1,0]
	v_pk_mul_f32 v[78:79], v[78:79], v[84:85] op_sel_hi:[1,0]
	v_pk_fma_f32 v[80:81], v[2:3], v[80:81], v[6:7]
	v_pk_fma_f32 v[78:79], v[4:5], v[78:79], v[8:9]
	v_cvt_pk_bf16_f32 v80, v80, v81
	v_cvt_pk_bf16_f32 v81, v78, v79
	global_store_dwordx2 v[74:75], v[80:81], off offset:1536
	ds_write2st64_b64 v85, v[76:77], v[80:81] offset0:58 offset1:59
	v_lshlrev_b32_e32 v80, 16, v63
	v_and_b32_e32 v81, 0xffff0000, v63
	v_lshlrev_b32_e32 v82, 16, v65
	v_and_b32_e32 v83, 0xffff0000, v65
	v_pk_fma_f32 v[80:81], v[80:81], s[2:3], v[82:83] op_sel_hi:[1,0,1]
	v_lshlrev_b32_e32 v82, 16, v62
	v_and_b32_e32 v83, 0xffff0000, v62
	v_lshlrev_b32_e32 v62, 16, v64
	v_and_b32_e32 v63, 0xffff0000, v64
	global_store_dwordx2 v[74:75], v[86:87], off offset:512
	global_store_dwordx2 v[74:75], v[76:77], off offset:1024
	v_lshlrev_b32_e32 v74, 16, v70
	v_and_b32_e32 v75, 0xffff0000, v70
	v_lshlrev_b32_e32 v76, 16, v72
	v_and_b32_e32 v77, 0xffff0000, v72
	v_and_b32_e32 v70, 0xffff0000, v71
	v_lshlrev_b32_e32 v71, 16, v71
	v_and_b32_e32 v72, 0xffff0000, v73
	v_lshlrev_b32_e32 v73, 16, v73
	v_pk_fma_f32 v[62:63], v[82:83], s[2:3], v[62:63] op_sel_hi:[1,0,1]
	v_pk_fma_f32 v[74:75], v[74:75], s[2:3], v[76:77] op_sel_hi:[1,0,1]
	v_pk_fma_f32 v[70:71], v[70:71], s[2:3], v[72:73] op_sel_hi:[1,0,1]
	v_lshlrev_b32_e32 v72, 16, v66
	v_and_b32_e32 v66, 0xffff0000, v66
	v_mov_b32_e32 v64, v62
	v_mov_b32_e32 v65, v81
	v_pk_mov_b32 v[82:83], v[62:63], v[80:81] op_sel:[1,0]
	v_lshlrev_b32_e32 v73, 16, v68
	v_mul_f32_e32 v66, 0x3fd744fd, v66
	v_and_b32_e32 v68, 0xffff0000, v68
	v_pk_add_f32 v[64:65], v[64:65], v[82:83]
	v_pk_add_f32 v[82:83], v[74:75], v[74:75] op_sel:[0,1] op_sel_hi:[1,0]
	v_pk_add_f32 v[84:85], v[70:71], v[70:71] op_sel:[0,1] op_sel_hi:[1,0]
	v_mov_b32_e32 v83, v66
	v_mov_b32_e32 v85, v68
	v_pk_add_f32 v[82:83], v[82:83], v[84:85]
	v_lshlrev_b32_e32 v84, 16, v59
	v_and_b32_e32 v85, 0xffff0000, v59
	v_lshlrev_b32_e32 v86, 16, v61
	v_and_b32_e32 v87, 0xffff0000, v61
	v_lshlrev_b32_e32 v76, 16, v67
	v_pk_fma_f32 v[84:85], v[84:85], s[2:3], v[86:87] op_sel_hi:[1,0,1]
	v_mul_f32_e32 v77, 0x3fd744fd, v76
	v_lshlrev_b32_e32 v79, 16, v69
	v_mov_b32_e32 v76, v85
	v_mov_b32_e32 v78, v84
	v_pk_add_f32 v[76:77], v[76:77], v[78:79]
	v_lshlrev_b32_e32 v78, 16, v58
	v_and_b32_e32 v79, 0xffff0000, v58
	v_lshlrev_b32_e32 v58, 16, v60
	v_and_b32_e32 v59, 0xffff0000, v60
	v_mul_f32_e32 v72, 0x3fd744fd, v72
	v_and_b32_e32 v67, 0xffff0000, v67
	v_pk_add_f32 v[64:65], v[64:65], v[64:65] op_sel:[0,1] op_sel_hi:[1,0]
	v_pk_fma_f32 v[58:59], v[78:79], s[2:3], v[58:59] op_sel_hi:[1,0,1]
	v_mul_f32_e32 v67, 0x3fd744fd, v67
	v_and_b32_e32 v69, 0xffff0000, v69
	v_mov_b32_e32 v65, v72
	v_mov_b32_e32 v72, v1
	v_mov_b32_e32 v66, v58
	v_mov_b32_e32 v68, v59
	v_pk_add_f32 v[64:65], v[64:65], v[72:73]
	v_pk_add_f32 v[60:61], v[66:67], v[68:69]
	v_pk_add_f32 v[72:73], v[64:65], v[82:83]
	v_pk_add_f32 v[66:67], v[60:61], v[76:77]
	v_mov_b32_e32 v82, v65
	v_pk_add_f32 v[66:67], v[72:73], v[66:67]
	s_nop 0
	v_add_f32_e32 v60, v66, v67
	s_nop 1
	v_add_f32_dpp v60, v60, v60 quad_perm:[1,0,3,2] row_mask:0xf bank_mask:0xf bound_ctrl:1
	s_nop 1
	v_add_f32_dpp v60, v60, v60 quad_perm:[2,3,0,1] row_mask:0xf bank_mask:0xf bound_ctrl:1
	s_nop 1
	v_add_f32_dpp v60, v60, v60 row_half_mirror row_mask:0xf bank_mask:0xf bound_ctrl:1
	s_nop 1
	v_add_f32_dpp v60, v60, v60 row_mirror row_mask:0xf bank_mask:0xf bound_ctrl:1
	v_mov_b32_e32 v64, v60
	s_nop 1
	v_permlane32_swap_b32 v60, v64
	s_nop 0
	v_add_f32_e32 v60, v60, v64
	v_mov_b32_e32 v64, v60
	s_nop 1
	v_permlane16_swap_b32_e32 v60, v64
	s_waitcnt lgkmcnt(0)
	v_add_f32_e32 v60, v60, v64
	v_mul_f32_e32 v64, 0x3a800000, v60
	v_pk_add_f32 v[62:63], v[62:63], v[64:65] op_sel_hi:[1,0] neg_lo:[0,1] neg_hi:[0,1]
	v_pk_add_f32 v[68:69], v[80:81], v[64:65] op_sel_hi:[1,0] neg_lo:[0,1] neg_hi:[0,1]
	v_pk_mul_f32 v[66:67], v[62:63], v[62:63]
	v_pk_mul_f32 v[72:73], v[68:69], v[68:69]
	v_add_f32_e32 v66, v66, v67
	v_pk_add_f32 v[74:75], v[74:75], v[64:65] op_sel_hi:[1,0] neg_lo:[0,1] neg_hi:[0,1]
	v_add_f32_e32 v66, v72, v66
	v_pk_mul_f32 v[88:89], v[74:75], v[74:75]
	v_add_f32_e32 v66, v73, v66
	v_pk_add_f32 v[70:71], v[70:71], v[64:65] op_sel_hi:[1,0] neg_lo:[0,1] neg_hi:[0,1]
	v_add_f32_e32 v66, v88, v66
	v_pk_mul_f32 v[86:87], v[70:71], v[70:71]
	v_add_f32_e32 v66, v89, v66
	v_pk_add_f32 v[58:59], v[58:59], v[64:65] op_sel_hi:[1,0] neg_lo:[0,1] neg_hi:[0,1]
	v_add_f32_e32 v66, v87, v66
	v_pk_mul_f32 v[78:79], v[58:59], v[58:59]
	v_add_f32_e32 v66, v86, v66
	v_pk_add_f32 v[80:81], v[84:85], v[64:65] op_sel_hi:[1,0] neg_lo:[0,1] neg_hi:[0,1]
	v_add_f32_e32 v66, v78, v66
	v_pk_mul_f32 v[84:85], v[80:81], v[80:81]
	v_mov_b32_e32 v60, v77
	v_add_f32_e32 v66, v79, v66
	v_pk_add_f32 v[60:61], v[60:61], v[64:65] op_sel_hi:[1,0] neg_lo:[0,1] neg_hi:[0,1]
	v_pk_add_f32 v[64:65], v[82:83], v[64:65] op_sel_hi:[1,0] neg_lo:[0,1] neg_hi:[0,1]
	v_add_f32_e32 v66, v84, v66
	v_pk_mul_f32 v[82:83], v[64:65], v[64:65]
	v_add_f32_e32 v66, v85, v66
	v_add_f32_e32 v66, v82, v66
	v_pk_mul_f32 v[76:77], v[60:61], v[60:61]
	v_add_f32_e32 v66, v83, v66
	v_add_f32_e32 v66, v76, v66
	v_add_f32_e32 v66, v77, v66
	s_nop 1
	v_add_f32_dpp v66, v66, v66 quad_perm:[1,0,3,2] row_mask:0xf bank_mask:0xf bound_ctrl:1
	s_nop 1
	v_add_f32_dpp v66, v66, v66 quad_perm:[2,3,0,1] row_mask:0xf bank_mask:0xf bound_ctrl:1
	s_nop 1
	v_add_f32_dpp v66, v66, v66 row_half_mirror row_mask:0xf bank_mask:0xf bound_ctrl:1
	s_nop 1
	v_add_f32_dpp v66, v66, v66 row_mirror row_mask:0xf bank_mask:0xf bound_ctrl:1
	v_mov_b32_e32 v67, v66
	s_nop 1
	v_permlane32_swap_b32 v66, v67
	s_nop 0
	v_add_f32_e32 v66, v66, v67
	v_mov_b32_e32 v67, v66
	s_nop 1
	v_permlane16_swap_b32_e32 v66, v67
	s_waitcnt lgkmcnt(0)
	v_add_f32_e32 v66, v66, v67
	v_fmamk_f32 v66, v66, 0x3a800000, v206
	v_mul_f32_e32 v67, 0x4f800000, v66
	v_cmp_gt_f32_e32 vcc, s45, v66
	s_nop 1
	v_cndmask_b32_e32 v66, v66, v67, vcc
	v_sqrt_f32_e32 v67, v66
	s_nop 0
	v_add_u32_e32 v72, -1, v67
	v_fma_f32 v73, -v72, v67, v66
	v_cmp_ge_f32_e64 s[0:1], 0, v73
	v_add_u32_e32 v73, 1, v67
	s_nop 0
	v_cndmask_b32_e64 v72, v67, v72, s[0:1]
	v_fma_f32 v67, -v73, v67, v66
	v_cmp_lt_f32_e64 s[0:1], 0, v67
	s_nop 1
	v_cndmask_b32_e64 v67, v72, v73, s[0:1]
	v_mul_f32_e32 v72, 0x37800000, v67
	v_cndmask_b32_e32 v67, v67, v72, vcc
	v_cmp_class_f32_e32 vcc, v66, v207
	s_nop 1
	v_cndmask_b32_e32 v66, v67, v66, vcc
	v_div_scale_f32 v67, s[0:1], v66, v66, 1.0
	v_rcp_f32_e32 v72, v67
	s_mov_b64 s[0:1], 0
	v_fma_f32 v73, -v67, v72, 1.0
	v_fmac_f32_e32 v72, v73, v72
	v_div_scale_f32 v73, vcc, 1.0, v66, 1.0
	v_mul_f32_e32 v76, v73, v72
	v_fma_f32 v77, -v67, v76, v73
	v_fmac_f32_e32 v76, v77, v72
	v_fma_f32 v67, -v67, v76, v73
	v_div_fmas_f32 v67, v67, v72, v76
	v_div_fixup_f32 v66, v67, v66, 1.0
	v_pk_mul_f32 v[62:63], v[62:63], v[66:67] op_sel_hi:[1,0]
	s_nop 0
	v_pk_fma_f32 v[26:27], v[26:27], v[62:63], v[30:31]
	v_pk_mul_f32 v[30:31], v[68:69], v[66:67] op_sel_hi:[1,0]
	v_cvt_pk_bf16_f32 v26, v26, v27
	v_pk_fma_f32 v[28:29], v[28:29], v[30:31], v[32:33]
	s_nop 0
	v_cvt_pk_bf16_f32 v27, v28, v29
	v_pk_mul_f32 v[28:29], v[74:75], v[66:67] op_sel_hi:[1,0]
	global_store_dwordx2 v[56:57], v[26:27], off
	v_pk_fma_f32 v[18:19], v[18:19], v[28:29], v[22:23]
	v_pk_mul_f32 v[22:23], v[70:71], v[66:67] op_sel_hi:[1,0]
	v_cvt_pk_bf16_f32 v18, v18, v19
	v_pk_fma_f32 v[20:21], v[20:21], v[22:23], v[24:25] op_sel:[0,1,0] op_sel_hi:[1,0,1]
	s_nop 0
	v_cvt_pk_bf16_f32 v19, v20, v21
	v_add_u32_e32 v20, 0x70, v195
	global_store_dwordx2 v[56:57], v[18:19], off offset:512
	ds_write2st64_b64 v20, v[26:27], v[18:19] offset0:60 offset1:61
	v_pk_mul_f32 v[18:19], v[58:59], v[66:67] op_sel_hi:[1,0]
	s_nop 0
	v_pk_fma_f32 v[10:11], v[10:11], v[18:19], v[14:15]
	v_pk_mul_f32 v[14:15], v[80:81], v[66:67] op_sel_hi:[1,0]
	v_cvt_pk_bf16_f32 v10, v10, v11
	v_pk_fma_f32 v[12:13], v[12:13], v[14:15], v[16:17]
	s_nop 0
	v_cvt_pk_bf16_f32 v11, v12, v13
	v_pk_mul_f32 v[12:13], v[64:65], v[66:67] op_sel_hi:[1,0]
	global_store_dwordx2 v[56:57], v[10:11], off offset:1024
	v_pk_fma_f32 v[2:3], v[2:3], v[12:13], v[6:7]
	v_pk_mul_f32 v[6:7], v[60:61], v[66:67] op_sel_hi:[1,0]
	v_cvt_pk_bf16_f32 v2, v2, v3
	v_pk_fma_f32 v[4:5], v[4:5], v[6:7], v[8:9]
	s_nop 0
	v_cvt_pk_bf16_f32 v3, v4, v5
	global_store_dwordx2 v[56:57], v[2:3], off offset:1536
	ds_write2st64_b64 v20, v[10:11], v[2:3] offset0:62 offset1:63
	v_mov_b32_e32 v2, 0
	v_mov_b32_e32 v10, v0
	v_mov_b32_e32 v3, v2
	v_mov_b32_e32 v4, v2
	v_mov_b32_e32 v5, v2
	s_waitcnt lgkmcnt(0)
	s_barrier

.LBB0_2147:
	s_or_b64 exec, exec, s[2:3]
	v_lshlrev_b32_e32 v54, 16, v146
	v_and_b32_e32 v55, 0xffff0000, v146
	v_lshlrev_b32_e32 v56, 16, v147
	v_and_b32_e32 v57, 0xffff0000, v147
	v_lshlrev_b32_e32 v146, 16, v144
	v_and_b32_e32 v147, 0xffff0000, v144
	v_pk_fma_f32 v[54:55], v[46:47], v[54:55], 0 op_sel_hi:[0,1,0]
	v_pk_fma_f32 v[54:55], v[46:47], v[146:147], v[54:55] op_sel:[1,0,0]
	v_lshlrev_b32_e32 v146, 16, v140
	v_and_b32_e32 v147, 0xffff0000, v140
	v_pk_fma_f32 v[54:55], v[48:49], v[146:147], v[54:55] op_sel_hi:[0,1,1]
	v_lshlrev_b32_e32 v146, 16, v142
	v_and_b32_e32 v147, 0xffff0000, v142
	v_mov_b32_e32 v0, v49
	v_lshlrev_b32_e32 v144, 16, v145
	v_and_b32_e32 v145, 0xffff0000, v145
	v_lshlrev_b32_e32 v150, 16, v138
	v_and_b32_e32 v151, 0xffff0000, v138
	v_pk_fma_f32 v[54:55], v[0:1], v[146:147], v[54:55] op_sel_hi:[0,1,1]
	s_mov_b32 s2, 0x3fd744fd
	v_pk_fma_f32 v[56:57], v[46:47], v[56:57], 0 op_sel_hi:[0,1,0]
	v_pk_fma_f32 v[146:147], v[150:151], s[2:3], v[54:55] op_sel_hi:[1,0,1]
	v_lshlrev_b32_e32 v54, 16, v139
	v_and_b32_e32 v55, 0xffff0000, v139
	v_pk_fma_f32 v[56:57], v[46:47], v[144:145], v[56:57] op_sel:[1,0,0]
	v_lshlrev_b32_e32 v138, 16, v141
	v_and_b32_e32 v139, 0xffff0000, v141
	v_pk_fma_f32 v[56:57], v[48:49], v[138:139], v[56:57] op_sel_hi:[0,1,1]
	v_lshlrev_b32_e32 v138, 16, v143
	v_and_b32_e32 v139, 0xffff0000, v143
	v_pk_fma_f32 v[56:57], v[0:1], v[138:139], v[56:57] op_sel_hi:[0,1,1]
	v_pk_fma_f32 v[138:139], v[54:55], s[2:3], v[56:57] op_sel_hi:[1,0,1]
	v_add_f32_e32 v54, v146, v147
	v_add_f32_e32 v49, v139, v138
	v_add_f32_e32 v49, v54, v49
	v_lshlrev_b32_e32 v54, 16, v136
	v_and_b32_e32 v55, 0xffff0000, v136
	v_lshlrev_b32_e32 v56, 16, v137
	v_and_b32_e32 v57, 0xffff0000, v137
	v_lshlrev_b32_e32 v136, 16, v134
	v_and_b32_e32 v137, 0xffff0000, v134
	v_lshlrev_b32_e32 v134, 16, v135
	v_and_b32_e32 v135, 0xffff0000, v135
	v_pk_fma_f32 v[54:55], v[46:47], v[54:55], 0 op_sel_hi:[0,1,0]
	v_pk_fma_f32 v[56:57], v[46:47], v[56:57], 0 op_sel_hi:[0,1,0]
	v_add_f32_e32 v49, 0, v49
	v_pk_fma_f32 v[54:55], v[46:47], v[136:137], v[54:55] op_sel:[1,0,0]
	v_lshlrev_b32_e32 v136, 16, v130
	v_and_b32_e32 v137, 0xffff0000, v130
	v_pk_fma_f32 v[56:57], v[46:47], v[134:135], v[56:57] op_sel:[1,0,0]
	v_lshlrev_b32_e32 v130, 16, v131
	v_and_b32_e32 v131, 0xffff0000, v131
	v_pk_fma_f32 v[54:55], v[48:49], v[136:137], v[54:55] op_sel_hi:[0,1,1]
	v_lshlrev_b32_e32 v136, 16, v132
	v_and_b32_e32 v137, 0xffff0000, v132
	v_pk_fma_f32 v[56:57], v[48:49], v[130:131], v[56:57] op_sel_hi:[0,1,1]
	v_lshlrev_b32_e32 v130, 16, v133
	v_and_b32_e32 v131, 0xffff0000, v133
	v_lshlrev_b32_e32 v140, 16, v128
	v_and_b32_e32 v141, 0xffff0000, v128
	v_pk_fma_f32 v[54:55], v[0:1], v[136:137], v[54:55] op_sel_hi:[0,1,1]
	v_lshlrev_b32_e32 v128, 16, v129
	v_and_b32_e32 v129, 0xffff0000, v129
	v_pk_fma_f32 v[56:57], v[0:1], v[130:131], v[56:57] op_sel_hi:[0,1,1]
	v_pk_fma_f32 v[54:55], v[140:141], s[2:3], v[54:55] op_sel_hi:[1,0,1]
	v_pk_fma_f32 v[56:57], v[128:129], s[2:3], v[56:57] op_sel_hi:[1,0,1]
	v_add_f32_e32 v128, v54, v55
	v_add_f32_e32 v107, v57, v56
	v_add_f32_e32 v107, v128, v107
	v_lshlrev_b32_e32 v128, 16, v126
	v_and_b32_e32 v129, 0xffff0000, v126
	v_lshlrev_b32_e32 v126, 16, v127
	v_and_b32_e32 v127, 0xffff0000, v127
	v_lshlrev_b32_e32 v130, 16, v124
	v_and_b32_e32 v131, 0xffff0000, v124
	v_lshlrev_b32_e32 v124, 16, v125
	v_and_b32_e32 v125, 0xffff0000, v125
	v_pk_fma_f32 v[128:129], v[46:47], v[128:129], 0 op_sel_hi:[0,1,0]
	v_pk_fma_f32 v[126:127], v[46:47], v[126:127], 0 op_sel_hi:[0,1,0]
	v_add_f32_e32 v49, v107, v49
	v_pk_fma_f32 v[128:129], v[46:47], v[130:131], v[128:129] op_sel:[1,0,0]
	v_lshlrev_b32_e32 v130, 16, v118
	v_and_b32_e32 v131, 0xffff0000, v118
	v_pk_fma_f32 v[124:125], v[46:47], v[124:125], v[126:127] op_sel:[1,0,0]
	v_lshlrev_b32_e32 v118, 16, v119
	v_and_b32_e32 v119, 0xffff0000, v119
	v_pk_fma_f32 v[128:129], v[48:49], v[130:131], v[128:129] op_sel_hi:[0,1,1]
	v_lshlrev_b32_e32 v130, 16, v122
	v_and_b32_e32 v131, 0xffff0000, v122
	v_pk_fma_f32 v[118:119], v[48:49], v[118:119], v[124:125] op_sel_hi:[0,1,1]
	v_lshlrev_b32_e32 v122, 16, v123
	v_and_b32_e32 v123, 0xffff0000, v123
	v_lshlrev_b32_e32 v132, 16, v120
	v_and_b32_e32 v133, 0xffff0000, v120
	v_pk_fma_f32 v[128:129], v[0:1], v[130:131], v[128:129] op_sel_hi:[0,1,1]
	v_lshlrev_b32_e32 v120, 16, v121
	v_and_b32_e32 v121, 0xffff0000, v121
	v_pk_fma_f32 v[118:119], v[0:1], v[122:123], v[118:119] op_sel_hi:[0,1,1]
	v_pk_fma_f32 v[128:129], v[132:133], s[2:3], v[128:129] op_sel_hi:[1,0,1]
	v_pk_fma_f32 v[118:119], v[120:121], s[2:3], v[118:119] op_sel_hi:[1,0,1]
	v_add_f32_e32 v120, v128, v129
	v_add_f32_e32 v107, v119, v118
	v_add_f32_e32 v107, v120, v107
	v_lshlrev_b32_e32 v120, 16, v116
	v_and_b32_e32 v121, 0xffff0000, v116
	v_lshlrev_b32_e32 v116, 16, v117
	v_and_b32_e32 v117, 0xffff0000, v117
	v_lshlrev_b32_e32 v122, 16, v114
	v_and_b32_e32 v123, 0xffff0000, v114
	v_lshlrev_b32_e32 v114, 16, v115
	v_and_b32_e32 v115, 0xffff0000, v115
	v_pk_fma_f32 v[120:121], v[46:47], v[120:121], 0 op_sel_hi:[0,1,0]
	v_pk_fma_f32 v[116:117], v[46:47], v[116:117], 0 op_sel_hi:[0,1,0]
	v_pk_fma_f32 v[120:121], v[46:47], v[122:123], v[120:121] op_sel:[1,0,0]
	v_lshlrev_b32_e32 v122, 16, v108
	v_and_b32_e32 v123, 0xffff0000, v108
	v_pk_fma_f32 v[46:47], v[46:47], v[114:115], v[116:117] op_sel:[1,0,0]
	v_lshlrev_b32_e32 v108, 16, v109
	v_and_b32_e32 v109, 0xffff0000, v109
	v_add_f32_e32 v107, v107, v49
	v_pk_fma_f32 v[120:121], v[48:49], v[122:123], v[120:121] op_sel_hi:[0,1,1]
	v_lshlrev_b32_e32 v122, 16, v110
	v_and_b32_e32 v123, 0xffff0000, v110
	v_pk_fma_f32 v[46:47], v[48:49], v[108:109], v[46:47] op_sel_hi:[0,1,1]
	v_lshlrev_b32_e32 v48, 16, v111
	v_and_b32_e32 v49, 0xffff0000, v111
	v_lshlrev_b32_e32 v124, 16, v112
	v_and_b32_e32 v125, 0xffff0000, v112
	v_pk_fma_f32 v[120:121], v[0:1], v[122:123], v[120:121] op_sel_hi:[0,1,1]
	v_lshlrev_b32_e32 v112, 16, v113
	v_and_b32_e32 v113, 0xffff0000, v113
	v_pk_fma_f32 v[46:47], v[0:1], v[48:49], v[46:47] op_sel_hi:[0,1,1]
	v_pk_fma_f32 v[120:121], v[124:125], s[2:3], v[120:121] op_sel_hi:[1,0,1]
	v_pk_fma_f32 v[46:47], v[112:113], s[2:3], v[46:47] op_sel_hi:[1,0,1]
	v_add_f32_e32 v48, v120, v121
	v_add_f32_e32 v0, v47, v46
	v_add_f32_e32 v0, v48, v0
	v_add_f32_e32 v0, v0, v107
	s_nop 1
	v_add_f32_dpp v0, v0, v0 quad_perm:[1,0,3,2] row_mask:0xf bank_mask:0xf bound_ctrl:1
	s_nop 1
	v_add_f32_dpp v0, v0, v0 quad_perm:[2,3,0,1] row_mask:0xf bank_mask:0xf bound_ctrl:1
	s_nop 1
	v_add_f32_dpp v0, v0, v0 row_half_mirror row_mask:0xf bank_mask:0xf bound_ctrl:1
	s_nop 1
	v_add_f32_dpp v0, v0, v0 row_mirror row_mask:0xf bank_mask:0xf bound_ctrl:1
	v_mov_b32_e32 v48, v0
	s_nop 1
	v_permlane32_swap_b32 v0, v48
	s_nop 0
	v_add_f32_e32 v0, v0, v48
	v_mov_b32_e32 v48, v0
	s_nop 1
	v_permlane16_swap_b32_e32 v0, v48
	s_waitcnt lgkmcnt(0)
	v_add_f32_e32 v0, v0, v48
	v_mul_f32_e32 v0, 0x3a800000, v0
	v_pk_add_f32 v[124:125], v[146:147], v[0:1] op_sel_hi:[1,0] neg_lo:[0,1] neg_hi:[0,1]
	v_pk_add_f32 v[108:109], v[128:129], v[0:1] op_sel_hi:[1,0] neg_lo:[0,1] neg_hi:[0,1]
	v_pk_mul_f32 v[126:127], v[124:125], v[124:125]
	v_pk_add_f32 v[128:129], v[138:139], v[0:1] op_sel_hi:[1,0] neg_lo:[0,1] neg_hi:[0,1]
	v_pk_add_f32 v[112:113], v[54:55], v[0:1] op_sel_hi:[1,0] neg_lo:[0,1] neg_hi:[0,1]
	v_pk_add_f32 v[114:115], v[56:57], v[0:1] op_sel_hi:[1,0] neg_lo:[0,1] neg_hi:[0,1]
	v_pk_add_f32 v[110:111], v[118:119], v[0:1] op_sel_hi:[1,0] neg_lo:[0,1] neg_hi:[0,1]
	v_pk_add_f32 v[54:55], v[120:121], v[0:1] op_sel_hi:[1,0] neg_lo:[0,1] neg_hi:[0,1]
	v_pk_add_f32 v[56:57], v[46:47], v[0:1] op_sel_hi:[1,0] neg_lo:[0,1] neg_hi:[0,1]
	v_pk_mul_f32 v[130:131], v[128:129], v[128:129]
	v_add_f32_e32 v0, v126, v127
	v_add_f32_e32 v0, v130, v0
	v_pk_mul_f32 v[48:49], v[112:113], v[112:113]
	v_add_f32_e32 v0, v131, v0
	v_add_f32_e32 v0, v48, v0
	v_pk_mul_f32 v[116:117], v[114:115], v[114:115]
	v_add_f32_e32 v0, v49, v0
	v_add_f32_e32 v0, v116, v0
	v_pk_mul_f32 v[122:123], v[108:109], v[108:109]
	v_add_f32_e32 v0, v117, v0
	v_add_f32_e32 v0, v122, v0
	v_pk_mul_f32 v[118:119], v[110:111], v[110:111]
	v_add_f32_e32 v0, v123, v0
	v_add_f32_e32 v0, v118, v0
	v_pk_mul_f32 v[120:121], v[54:55], v[54:55]
	v_add_f32_e32 v0, v119, v0
	v_add_f32_e32 v0, v120, v0
	v_pk_mul_f32 v[46:47], v[56:57], v[56:57]
	v_add_f32_e32 v0, v121, v0
	v_add_f32_e32 v0, v46, v0
	v_add_f32_e32 v0, v47, v0
	s_nop 1
	v_add_f32_dpp v0, v0, v0 quad_perm:[1,0,3,2] row_mask:0xf bank_mask:0xf bound_ctrl:1
	s_nop 1
	v_add_f32_dpp v0, v0, v0 quad_perm:[2,3,0,1] row_mask:0xf bank_mask:0xf bound_ctrl:1
	s_nop 1
	v_add_f32_dpp v0, v0, v0 row_half_mirror row_mask:0xf bank_mask:0xf bound_ctrl:1
	s_nop 1
	v_add_f32_dpp v0, v0, v0 row_mirror row_mask:0xf bank_mask:0xf bound_ctrl:1
	v_mov_b32_e32 v46, v0
	s_nop 1
	v_permlane32_swap_b32 v0, v46
	s_nop 0
	v_add_f32_e32 v0, v0, v46
	v_mov_b32_e32 v46, v0
	s_nop 1
	v_permlane16_swap_b32_e32 v0, v46
	s_waitcnt lgkmcnt(0)
	v_add_f32_e32 v0, v0, v46
	v_fmamk_f32 v0, v0, 0x3a800000, v206
	v_mul_f32_e32 v46, 0x4f800000, v0
	v_cmp_gt_f32_e32 vcc, s45, v0
	s_nop 1
	v_cndmask_b32_e32 v0, v0, v46, vcc
	v_sqrt_f32_e32 v46, v0
	s_nop 0
	v_add_u32_e32 v47, -1, v46
	v_fma_f32 v48, -v47, v46, v0
	v_cmp_ge_f32_e64 s[2:3], 0, v48
	v_add_u32_e32 v48, 1, v46
	s_nop 0
	v_cndmask_b32_e64 v47, v46, v47, s[2:3]
	v_fma_f32 v46, -v48, v46, v0
	v_cmp_lt_f32_e64 s[2:3], 0, v46
	s_nop 1
	v_cndmask_b32_e64 v46, v47, v48, s[2:3]
	v_mul_f32_e32 v47, 0x37800000, v46
	v_cndmask_b32_e32 v46, v46, v47, vcc
	v_cmp_class_f32_e32 vcc, v0, v207
	s_nop 1
	v_cndmask_b32_e32 v0, v46, v0, vcc
	v_div_scale_f32 v46, s[2:3], v0, v0, 1.0
	v_rcp_f32_e32 v47, v46
	s_mov_b64 s[2:3], -1
	v_fma_f32 v48, -v46, v47, 1.0
	v_fmac_f32_e32 v47, v48, v47
	v_div_scale_f32 v48, vcc, 1.0, v0, 1.0
	v_mul_f32_e32 v49, v48, v47
	v_fma_f32 v107, -v46, v49, v48
	v_fmac_f32_e32 v49, v107, v47
	v_fma_f32 v46, -v46, v49, v48
	v_div_fmas_f32 v46, v46, v47, v49
	v_div_fixup_f32 v116, v46, v0, 1.0
	v_pk_mul_f32 v[46:47], v[124:125], v[116:117] op_sel_hi:[1,0]
	v_pk_mul_f32 v[48:49], v[128:129], v[116:117] op_sel_hi:[1,0]
	v_pk_fma_f32 v[46:47], v[6:7], v[46:47], v[22:23]
	v_pk_fma_f32 v[48:49], v[8:9], v[48:49], v[24:25]
	s_and_b64 vcc, exec, s[12:13]
	s_cbranch_vccz .LBB0_2149
	v_cvt_pk_bf16_f32 v118, v46, v47
	v_cvt_pk_bf16_f32 v119, v48, v49
	global_store_dwordx2 v[64:65], v[118:119], off offset:-1024
	s_mov_b64 s[2:3], 0
